# swiglu fp8 epilogues of P11 and P23 hand-written with packed f32 mul/add, in place on accumulators, saddr stores (same per-element operations)
# speedup vs baseline: 1.0171x; 1.0067x over previous
.LBB0_1390:
	s_add_u32 s14, s38, 0x3ac00000
	s_addc_u32 s15, s39, 0
	s_add_u32 s56, s38, 0xa4500000
	v_mov_b32_e32 v5, v174
	s_addc_u32 s57, s39, 0
	s_waitcnt vmcnt(2)
	s_barrier
	s_or_b32 s16, s93, 0x80
	s_add_i32 s58, s47, 0x18000
	s_mov_b32 m0, s58
	v_add_u32_e32 v5, s16, v5
	global_load_lds_dwordx4 v5, s[20:21]
	v_mov_b32_e32 v5, v174
	s_add_i32 s16, s16, s46
	s_add_i32 s59, s47, 0x1a000
	v_add_u32_e32 v5, s16, v5
	s_mov_b32 m0, s59
	s_or_b32 s16, s92, 0x80
	global_load_lds_dwordx4 v5, s[20:21]
	v_mov_b32_e32 v5, v1
	s_add_i32 s60, s47, 0x8000
	v_add_u32_e32 v5, s16, v5
	s_mov_b32 m0, s60
	s_add_i32 s16, s16, s45
	global_load_lds_dwordx4 v5, s[10:11]
	v_mov_b32_e32 v5, v1
	s_add_i32 s61, s47, 0xa000
	s_lshl_b32 s4, s4, 8
	v_add_u32_e32 v5, s16, v5
	s_mov_b32 m0, s61
	s_add_i32 s4, s93, s4
	global_load_lds_dwordx4 v5, s[10:11]
	v_mov_b32_e32 v5, v174
	s_addk_i32 s4, 0x80
	s_add_i32 s62, s47, 0x1c000
	s_mov_b32 m0, s62
	v_add_u32_e32 v5, s4, v5
	global_load_lds_dwordx4 v5, s[20:21]
	v_mov_b32_e32 v5, v174
	s_add_i32 s4, s4, s46
	s_add_i32 s63, s47, 0x1e000
	v_add_u32_e32 v5, s4, v5
	s_mov_b32 m0, s63
	s_ashr_i32 s4, s3, 31
	global_load_lds_dwordx4 v5, s[20:21]
	s_lshr_b32 s4, s4, 26
	s_and_b32 s5, s5, 3
	s_add_i32 s4, s3, s4
	s_ashr_i32 s64, s4, 6
	s_lshl_b32 s66, s9, 6
	s_lshl_b32 s4, s9, 13
	s_lshl_b32 s9, s5, 12
	v_and_b32_e32 v175, 15, v2
	s_lshl_b32 s65, s74, 8
	v_and_b32_e32 v5, 48, v2
	s_lshl_b32 s16, s5, 5
	v_lshlrev_b32_e32 v2, 2, v2
	s_add_i32 s9, s9, 0
	v_lshlrev_b32_e32 v6, 6, v175
	v_and_b32_e32 v2, 32, v2
	s_cmp_gt_i32 s3, 63
	v_bitop3_b32 v2, v6, v2, v5 bitop3:0x36
	s_cselect_b64 s[18:19], -1, 0
	s_add_i32 s67, s64, -2
	v_add_u32_e32 v5, 0, v2
	v_add_u32_e32 v6, s9, v2
	v_lshlrev_b32_e32 v2, 2, v3
	s_cmpk_lt_u32 s2, 0x100
	s_waitcnt vmcnt(6)
	v_and_b32_e32 v2, 0x7c, v2
	s_cselect_b64 s[22:23], -1, 0
	s_lshl_b32 s3, s5, 7
	s_and_b32 s2, s2, 0xffffff00
	s_mov_b32 s17, 0
	v_mul_u32_u24_e32 v4, 0x1600, v4
	s_lshl_b32 s5, s5, 6
	s_add_i32 s72, s3, 0
	s_add_i32 s73, s2, 0
	v_lshlrev_b32_e32 v168, 2, v2
	v_mbcnt_lo_u32_b32 v2, -1, 0
	v_lshrrev_b32_e32 v176, 4, v3
	v_mov_b32_e32 v163, 0
	s_movk_i32 s68, 0x1600
	v_add_u32_e32 v177, 0x10000, v6
	v_add_u32_e32 v178, 0x10400, v6
	v_add_u32_e32 v179, 0x14000, v6
	v_add_u32_e32 v180, 0x14400, v6
	v_add_u32_e32 v181, 0x18000, v6
	v_add_u32_e32 v182, 0x18400, v6
	v_add_u32_e32 v183, 0x1c000, v6
	v_add_u32_e32 v184, 0x1c400, v6
	s_or_b32 s69, s5, s2
	s_ashr_i32 s70, s66, 31
	v_add_u32_e32 v185, 0x10800, v6
	v_add_u32_e32 v186, 0x10c00, v6
	v_add_u32_e32 v187, 0x14800, v6
	v_add_u32_e32 v188, 0x14c00, v6
	v_add_u32_e32 v189, 0x18800, v6
	v_add_u32_e32 v190, 0x18c00, v6
	v_add_u32_e32 v191, 0x1c800, v6
	v_add_u32_e32 v192, 0x1cc00, v6
	s_ashr_i32 s71, s34, 31
	s_add_i32 s72, s72, 0x21400
	s_add_i32 s73, s73, 0x21000
	s_mulk_i32 s74, 0x180
	s_mov_b32 s28, -1
	v_mov_b64_e32 v[164:165], 0x16b0
	v_mov_b64_e32 v[166:167], 0x16af
	s_movk_i32 s76, 0x2d7
	v_lshlrev_b32_e32 v170, 2, v4
	v_add_u32_e32 v193, s4, v5
	v_mov_b32_e32 v194, 0x358637bd
	s_mov_b32 s77, 0x800000
	s_mov_b32 s24, 0x41000000
	s_mov_b32 s78, 0xc3e00000
	s_mov_b32 s79, 0x2c000
	s_mov_b32 s80, 0x42000
	s_mov_b32 s81, 0xb0000
	s_mov_b32 s82, 0xc6000
	s_mov_b32 s83, 0xdc000
	v_mbcnt_hi_u32_b32 v195, -1, v2
	v_mov_b32_e32 v196, 0x43e00000
	s_mov_b32 s9, s17
	s_mov_b32 s84, s17
	s_barrier
	s_branch .LBB0_1393
.Lzs_5:
	v_mov_b64_e32 v[34:35], 0
	v_mov_b64_e32 v[36:37], 0
	v_mov_b64_e32 v[38:39], 0
	v_mov_b64_e32 v[40:41], 0
	v_mov_b64_e32 v[42:43], 0
	v_mov_b64_e32 v[44:45], 0
	v_mov_b64_e32 v[46:47], 0
	v_mov_b64_e32 v[48:49], 0
	v_mov_b64_e32 v[50:51], 0
	v_mov_b64_e32 v[52:53], 0
	v_mov_b64_e32 v[54:55], 0
	v_mov_b64_e32 v[56:57], 0
	v_mov_b64_e32 v[58:59], 0
	v_mov_b64_e32 v[60:61], 0
	v_mov_b64_e32 v[62:63], 0
	v_mov_b64_e32 v[64:65], 0
	v_mov_b64_e32 v[66:67], 0
	v_mov_b64_e32 v[68:69], 0
	v_mov_b64_e32 v[70:71], 0
	v_mov_b64_e32 v[72:73], 0
	v_mov_b64_e32 v[74:75], 0
	v_mov_b64_e32 v[76:77], 0
	v_mov_b64_e32 v[78:79], 0
	v_mov_b64_e32 v[80:81], 0
	v_mov_b64_e32 v[82:83], 0
	v_mov_b64_e32 v[84:85], 0
	v_mov_b64_e32 v[86:87], 0
	v_mov_b64_e32 v[88:89], 0
	v_mov_b64_e32 v[90:91], 0
	v_mov_b64_e32 v[92:93], 0
	v_mov_b64_e32 v[94:95], 0
	v_mov_b64_e32 v[96:97], 0
	v_mov_b64_e32 v[98:99], 0
	v_mov_b64_e32 v[100:101], 0
	v_mov_b64_e32 v[102:103], 0
	v_mov_b64_e32 v[104:105], 0
	v_mov_b64_e32 v[106:107], 0
	v_mov_b64_e32 v[108:109], 0
	v_mov_b64_e32 v[110:111], 0
	v_mov_b64_e32 v[112:113], 0
	v_mov_b64_e32 v[114:115], 0
	v_mov_b64_e32 v[116:117], 0
	v_mov_b64_e32 v[118:119], 0
	v_mov_b64_e32 v[120:121], 0
	v_mov_b64_e32 v[122:123], 0
	v_mov_b64_e32 v[124:125], 0
	v_mov_b64_e32 v[126:127], 0
	v_mov_b64_e32 v[128:129], 0
	v_mov_b64_e32 v[130:131], 0
	v_mov_b64_e32 v[132:133], 0
	v_mov_b64_e32 v[134:135], 0
	v_mov_b64_e32 v[136:137], 0
	v_mov_b64_e32 v[138:139], 0
	v_mov_b64_e32 v[140:141], 0
	v_mov_b64_e32 v[142:143], 0
	v_mov_b64_e32 v[144:145], 0
	v_mov_b64_e32 v[146:147], 0
	v_mov_b64_e32 v[148:149], 0
	v_mov_b64_e32 v[150:151], 0
	v_mov_b64_e32 v[152:153], 0
	v_mov_b64_e32 v[154:155], 0
	v_mov_b64_e32 v[156:157], 0
	v_mov_b64_e32 v[158:159], 0
	v_mov_b64_e32 v[160:161], 0
	s_branch .LBB0_1400

.LBB0_1395:
	s_and_b32 s89, s84, 1
	s_andn2_b64 vcc, exec, s[18:19]
	s_cbranch_vccnz .Lzs_5
	s_min_i32 s30, s86, 0x80
	s_mul_hi_i32 s94, s85, 0x2e8ba2e9
	s_lshr_b32 s30, s30, 5
	s_lshr_b32 s95, s94, 31
	s_lshr_b32 s94, s94, 3
	s_mulk_i32 s30, 0x2c00
	s_add_i32 s94, s94, s95
	s_ashr_i32 s31, s30, 31
	s_mul_i32 s94, s94, 44
	s_lshl_b32 s75, s89, 10
	s_or_b64 s[4:5], s[4:5], s[6:7]
	s_sub_i32 s94, s85, s94
	s_lshl_b64 s[30:31], s[30:31], 2
	s_add_u32 s95, s25, s30
	s_addc_u32 s96, s35, s31
	s_lshl_b32 s30, s94, 7
	s_ashr_i32 s31, s30, 31
	s_lshl_b64 s[30:31], s[30:31], 2
	s_add_u32 s30, s95, s30
	s_addc_u32 s31, s96, s31
	v_mov_b32_e32 v169, v163
	v_lshl_add_u64 v[2:3], s[30:31], 0, v[168:169]
	v_mov_b32_e32 v171, v163
	s_add_i32 s95, s75, 0
	v_lshl_add_u64 v[172:173], v[2:3], 0, v[170:171]
	s_addk_i32 s92, 0x80
	s_addk_i32 s93, 0x100
	s_mov_b32 s94, 0
	s_add_i32 s95, s95, 0x21400
	v_mov_b64_e32 v[34:35], 0
	v_mov_b64_e32 v[36:37], 0
	v_mov_b64_e32 v[38:39], 0
	v_mov_b64_e32 v[40:41], 0
	v_mov_b64_e32 v[42:43], 0
	v_mov_b64_e32 v[44:45], 0
	v_mov_b64_e32 v[46:47], 0
	v_mov_b64_e32 v[48:49], 0
	v_mov_b64_e32 v[50:51], 0
	v_mov_b64_e32 v[52:53], 0
	v_mov_b64_e32 v[54:55], 0
	v_mov_b64_e32 v[56:57], 0
	v_mov_b64_e32 v[58:59], 0
	v_mov_b64_e32 v[60:61], 0
	v_mov_b64_e32 v[62:63], 0
	v_mov_b64_e32 v[64:65], 0
	v_mov_b64_e32 v[66:67], 0
	v_mov_b64_e32 v[68:69], 0
	v_mov_b64_e32 v[70:71], 0
	v_mov_b64_e32 v[72:73], 0
	v_mov_b64_e32 v[74:75], 0
	v_mov_b64_e32 v[76:77], 0
	v_mov_b64_e32 v[78:79], 0
	v_mov_b64_e32 v[80:81], 0
	v_mov_b64_e32 v[82:83], 0
	v_mov_b64_e32 v[84:85], 0
	v_mov_b64_e32 v[86:87], 0
	v_mov_b64_e32 v[88:89], 0
	v_mov_b64_e32 v[90:91], 0
	v_mov_b64_e32 v[92:93], 0
	v_mov_b64_e32 v[94:95], 0
	v_mov_b64_e32 v[96:97], 0
	v_mov_b64_e32 v[98:99], 0
	v_mov_b64_e32 v[100:101], 0
	v_mov_b64_e32 v[102:103], 0
	v_mov_b64_e32 v[104:105], 0
	v_mov_b64_e32 v[106:107], 0
	v_mov_b64_e32 v[108:109], 0
	v_mov_b64_e32 v[110:111], 0
	v_mov_b64_e32 v[112:113], 0
	v_mov_b64_e32 v[114:115], 0
	v_mov_b64_e32 v[116:117], 0
	v_mov_b64_e32 v[118:119], 0
	v_mov_b64_e32 v[120:121], 0
	v_mov_b64_e32 v[122:123], 0
	v_mov_b64_e32 v[124:125], 0
	v_mov_b64_e32 v[126:127], 0
	v_mov_b64_e32 v[128:129], 0
	v_mov_b64_e32 v[130:131], 0
	v_mov_b64_e32 v[132:133], 0
	v_mov_b64_e32 v[134:135], 0
	v_mov_b64_e32 v[136:137], 0
	v_mov_b64_e32 v[138:139], 0
	v_mov_b64_e32 v[140:141], 0
	v_mov_b64_e32 v[142:143], 0
	v_mov_b64_e32 v[144:145], 0
	v_mov_b64_e32 v[146:147], 0
	v_mov_b64_e32 v[148:149], 0
	v_mov_b64_e32 v[150:151], 0
	v_mov_b64_e32 v[152:153], 0
	v_mov_b64_e32 v[154:155], 0
	v_mov_b64_e32 v[156:157], 0
	v_mov_b64_e32 v[158:159], 0
	v_mov_b64_e32 v[160:161], 0
	s_branch .LBB0_1398

.LBB0_1408:
	s_mul_hi_i32 s4, s90, 0x2e8ba2e9
	s_lshr_b32 s5, s4, 31
	s_lshr_b32 s4, s4, 3
	s_add_i32 s4, s4, s5
	s_mul_i32 s4, s4, 44
	s_sub_i32 s4, s90, s4
	s_lshl_b32 s4, s4, 7
	s_waitcnt lgkmcnt(0)
	v_lshl_add_u32 v18, v175, 2, s73
	ds_read2_b32 v[28:29], v18 offset1:16
	ds_read2_b32 v[24:25], v18 offset0:32 offset1:48
	ds_read2_b32 v[22:23], v18 offset0:128 offset1:144
	ds_read2_b32 v[18:19], v18 offset0:160 offset1:176
	s_lshl_b32 s28, s30, 8
	s_add_i32 s28, s28, s66
	s_mul_i32 s28, s28, s68
	s_add_i32 s28, s28, s4
	s_add_i32 s28, s28, s16
	s_add_u32 s100, s14, s28
	s_addc_u32 s101, s15, 0
	s_mov_b32 s98, 0xbfb8aa3b
	v_mul_u32_u24_e32 v211, s68, v175
	v_lshl_add_u32 v211, v176, 3, v211
	v_pk_mul_f32 v[14:15], v[14:15], s[24:25] op_sel_hi:[1,0]
	v_pk_mul_f32 v[16:17], v[16:17], s[24:25] op_sel_hi:[1,0]
	v_pk_mul_f32 v[10:11], v[10:11], s[24:25] op_sel_hi:[1,0]
	v_pk_mul_f32 v[12:13], v[12:13], s[24:25] op_sel_hi:[1,0]
	s_waitcnt lgkmcnt(0)
	v_mul_f32_e32 v30, 0x39000000, v28
	v_mul_f32_e32 v32, 0x39000000, v29
	v_mul_f32_e32 v31, 0x41000000, v30
	v_mul_f32_e32 v33, 0x41000000, v32
	v_pk_fma_f32 v[158:159], v[158:159], v[30:31], v[6:7] op_sel_hi:[1,0,1]
	v_pk_fma_f32 v[160:161], v[160:161], v[30:31], v[8:9] op_sel_hi:[1,0,1]
	v_pk_fma_f32 v[150:151], v[150:151], v[30:31], v[2:3] op_sel_hi:[1,0,1]
	v_pk_fma_f32 v[152:153], v[152:153], v[30:31], v[4:5] op_sel_hi:[1,0,1]
	v_pk_fma_f32 v[154:155], v[154:155], v[30:31], v[14:15] op_sel:[0,1,0] op_sel_hi:[1,1,1]
	v_pk_fma_f32 v[156:157], v[156:157], v[30:31], v[16:17] op_sel:[0,1,0] op_sel_hi:[1,1,1]
	v_pk_fma_f32 v[146:147], v[146:147], v[30:31], v[10:11] op_sel:[0,1,0] op_sel_hi:[1,1,1]
	v_pk_fma_f32 v[148:149], v[148:149], v[30:31], v[12:13] op_sel:[0,1,0] op_sel_hi:[1,1,1]
	v_pk_fma_f32 v[142:143], v[142:143], v[32:33], v[6:7] op_sel_hi:[1,0,1]
	v_pk_fma_f32 v[144:145], v[144:145], v[32:33], v[8:9] op_sel_hi:[1,0,1]
	v_pk_fma_f32 v[134:135], v[134:135], v[32:33], v[2:3] op_sel_hi:[1,0,1]
	v_pk_fma_f32 v[136:137], v[136:137], v[32:33], v[4:5] op_sel_hi:[1,0,1]
	v_pk_fma_f32 v[138:139], v[138:139], v[32:33], v[14:15] op_sel:[0,1,0] op_sel_hi:[1,1,1]
	v_pk_fma_f32 v[140:141], v[140:141], v[32:33], v[16:17] op_sel:[0,1,0] op_sel_hi:[1,1,1]
	v_pk_fma_f32 v[130:131], v[130:131], v[32:33], v[10:11] op_sel:[0,1,0] op_sel_hi:[1,1,1]
	v_pk_fma_f32 v[132:133], v[132:133], v[32:33], v[12:13] op_sel:[0,1,0] op_sel_hi:[1,1,1]
	v_pk_mul_f32 v[238:239], v[158:159], s[98:99] op_sel_hi:[1,0]
	v_pk_mul_f32 v[240:241], v[160:161], s[98:99] op_sel_hi:[1,0]
	v_pk_mul_f32 v[242:243], v[150:151], s[98:99] op_sel_hi:[1,0]
	v_pk_mul_f32 v[244:245], v[152:153], s[98:99] op_sel_hi:[1,0]
	v_pk_mul_f32 v[246:247], v[142:143], s[98:99] op_sel_hi:[1,0]
	v_pk_mul_f32 v[248:249], v[144:145], s[98:99] op_sel_hi:[1,0]
	v_pk_mul_f32 v[250:251], v[134:135], s[98:99] op_sel_hi:[1,0]
	v_pk_mul_f32 v[252:253], v[136:137], s[98:99] op_sel_hi:[1,0]
	v_exp_f32_e32 v238, v238
	v_exp_f32_e32 v239, v239
	v_exp_f32_e32 v240, v240
	v_exp_f32_e32 v241, v241
	v_exp_f32_e32 v242, v242
	v_exp_f32_e32 v243, v243
	v_exp_f32_e32 v244, v244
	v_exp_f32_e32 v245, v245
	v_exp_f32_e32 v246, v246
	v_exp_f32_e32 v247, v247
	v_exp_f32_e32 v248, v248
	v_exp_f32_e32 v249, v249
	v_exp_f32_e32 v250, v250
	v_exp_f32_e32 v251, v251
	v_exp_f32_e32 v252, v252
	v_exp_f32_e32 v253, v253
	v_pk_add_f32 v[238:239], v[238:239], 1.0 op_sel_hi:[1,0]
	v_pk_add_f32 v[240:241], v[240:241], 1.0 op_sel_hi:[1,0]
	v_pk_add_f32 v[242:243], v[242:243], 1.0 op_sel_hi:[1,0]
	v_pk_add_f32 v[244:245], v[244:245], 1.0 op_sel_hi:[1,0]
	v_pk_add_f32 v[246:247], v[246:247], 1.0 op_sel_hi:[1,0]
	v_pk_add_f32 v[248:249], v[248:249], 1.0 op_sel_hi:[1,0]
	v_pk_add_f32 v[250:251], v[250:251], 1.0 op_sel_hi:[1,0]
	v_pk_add_f32 v[252:253], v[252:253], 1.0 op_sel_hi:[1,0]
	v_rcp_f32_e32 v238, v238
	v_rcp_f32_e32 v239, v239
	v_rcp_f32_e32 v240, v240
	v_rcp_f32_e32 v241, v241
	v_rcp_f32_e32 v242, v242
	v_rcp_f32_e32 v243, v243
	v_rcp_f32_e32 v244, v244
	v_rcp_f32_e32 v245, v245
	v_rcp_f32_e32 v246, v246
	v_rcp_f32_e32 v247, v247
	v_rcp_f32_e32 v248, v248
	v_rcp_f32_e32 v249, v249
	v_rcp_f32_e32 v250, v250
	v_rcp_f32_e32 v251, v251
	v_rcp_f32_e32 v252, v252
	v_rcp_f32_e32 v253, v253
	v_pk_mul_f32 v[238:239], v[158:159], v[238:239]
	v_pk_mul_f32 v[240:241], v[160:161], v[240:241]
	v_pk_mul_f32 v[242:243], v[150:151], v[242:243]
	v_pk_mul_f32 v[244:245], v[152:153], v[244:245]
	v_pk_mul_f32 v[246:247], v[142:143], v[246:247]
	v_pk_mul_f32 v[248:249], v[144:145], v[248:249]
	v_pk_mul_f32 v[250:251], v[134:135], v[250:251]
	v_pk_mul_f32 v[252:253], v[136:137], v[252:253]
	v_pk_mul_f32 v[154:155], v[154:155], v[238:239]
	v_pk_mul_f32 v[156:157], v[156:157], v[240:241]
	v_pk_mul_f32 v[146:147], v[146:147], v[242:243]
	v_pk_mul_f32 v[148:149], v[148:149], v[244:245]
	v_pk_mul_f32 v[138:139], v[138:139], v[246:247]
	v_pk_mul_f32 v[140:141], v[140:141], v[248:249]
	v_pk_mul_f32 v[130:131], v[130:131], v[250:251]
	v_pk_mul_f32 v[132:133], v[132:133], v[252:253]
	v_med3_f32 v154, v154, s78, v196
	v_med3_f32 v155, v155, s78, v196
	v_med3_f32 v156, v156, s78, v196
	v_med3_f32 v157, v157, s78, v196
	v_med3_f32 v146, v146, s78, v196
	v_med3_f32 v147, v147, s78, v196
	v_med3_f32 v148, v148, s78, v196
	v_med3_f32 v149, v149, s78, v196
	v_med3_f32 v138, v138, s78, v196
	v_med3_f32 v139, v139, s78, v196
	v_med3_f32 v140, v140, s78, v196
	v_med3_f32 v141, v141, s78, v196
	v_med3_f32 v130, v130, s78, v196
	v_med3_f32 v131, v131, s78, v196
	v_med3_f32 v132, v132, s78, v196
	v_med3_f32 v133, v133, s78, v196
	v_cvt_pk_fp8_f32 v206, v154, v155
	v_cvt_pk_fp8_f32 v207, v146, v147
	v_cvt_pk_fp8_f32 v208, v138, v139
	v_cvt_pk_fp8_f32 v209, v130, v131
	v_add_u32_e32 v26, 0x16000, v211
	v_cvt_pk_fp8_f32 v206, v156, v157 op_sel:[0,0,1]
	v_cvt_pk_fp8_f32 v207, v148, v149 op_sel:[0,0,1]
	v_cvt_pk_fp8_f32 v208, v140, v141 op_sel:[0,0,1]
	v_cvt_pk_fp8_f32 v209, v132, v133 op_sel:[0,0,1]
	s_nop 1
	global_store_dwordx2 v211, v[206:207], s[100:101]
	global_store_dwordx2 v26, v[208:209], s[100:101]
	v_mul_f32_e32 v30, 0x39000000, v24
	v_mul_f32_e32 v32, 0x39000000, v25
	v_mul_f32_e32 v31, 0x41000000, v30
	v_mul_f32_e32 v33, 0x41000000, v32
	v_pk_fma_f32 v[126:127], v[126:127], v[30:31], v[6:7] op_sel_hi:[1,0,1]
	v_pk_fma_f32 v[128:129], v[128:129], v[30:31], v[8:9] op_sel_hi:[1,0,1]
	v_pk_fma_f32 v[118:119], v[118:119], v[30:31], v[2:3] op_sel_hi:[1,0,1]
	v_pk_fma_f32 v[120:121], v[120:121], v[30:31], v[4:5] op_sel_hi:[1,0,1]
	v_pk_fma_f32 v[122:123], v[122:123], v[30:31], v[14:15] op_sel:[0,1,0] op_sel_hi:[1,1,1]
	v_pk_fma_f32 v[124:125], v[124:125], v[30:31], v[16:17] op_sel:[0,1,0] op_sel_hi:[1,1,1]
	v_pk_fma_f32 v[114:115], v[114:115], v[30:31], v[10:11] op_sel:[0,1,0] op_sel_hi:[1,1,1]
	v_pk_fma_f32 v[116:117], v[116:117], v[30:31], v[12:13] op_sel:[0,1,0] op_sel_hi:[1,1,1]
	v_pk_fma_f32 v[110:111], v[110:111], v[32:33], v[6:7] op_sel_hi:[1,0,1]
	v_pk_fma_f32 v[112:113], v[112:113], v[32:33], v[8:9] op_sel_hi:[1,0,1]
	v_pk_fma_f32 v[102:103], v[102:103], v[32:33], v[2:3] op_sel_hi:[1,0,1]
	v_pk_fma_f32 v[104:105], v[104:105], v[32:33], v[4:5] op_sel_hi:[1,0,1]
	v_pk_fma_f32 v[106:107], v[106:107], v[32:33], v[14:15] op_sel:[0,1,0] op_sel_hi:[1,1,1]
	v_pk_fma_f32 v[108:109], v[108:109], v[32:33], v[16:17] op_sel:[0,1,0] op_sel_hi:[1,1,1]
	v_pk_fma_f32 v[98:99], v[98:99], v[32:33], v[10:11] op_sel:[0,1,0] op_sel_hi:[1,1,1]
	v_pk_fma_f32 v[100:101], v[100:101], v[32:33], v[12:13] op_sel:[0,1,0] op_sel_hi:[1,1,1]
	v_pk_mul_f32 v[238:239], v[126:127], s[98:99] op_sel_hi:[1,0]
	v_pk_mul_f32 v[240:241], v[128:129], s[98:99] op_sel_hi:[1,0]
	v_pk_mul_f32 v[242:243], v[118:119], s[98:99] op_sel_hi:[1,0]
	v_pk_mul_f32 v[244:245], v[120:121], s[98:99] op_sel_hi:[1,0]
	v_pk_mul_f32 v[246:247], v[110:111], s[98:99] op_sel_hi:[1,0]
	v_pk_mul_f32 v[248:249], v[112:113], s[98:99] op_sel_hi:[1,0]
	v_pk_mul_f32 v[250:251], v[102:103], s[98:99] op_sel_hi:[1,0]
	v_pk_mul_f32 v[252:253], v[104:105], s[98:99] op_sel_hi:[1,0]
	v_exp_f32_e32 v238, v238
	v_exp_f32_e32 v239, v239
	v_exp_f32_e32 v240, v240
	v_exp_f32_e32 v241, v241
	v_exp_f32_e32 v242, v242
	v_exp_f32_e32 v243, v243
	v_exp_f32_e32 v244, v244
	v_exp_f32_e32 v245, v245
	v_exp_f32_e32 v246, v246
	v_exp_f32_e32 v247, v247
	v_exp_f32_e32 v248, v248
	v_exp_f32_e32 v249, v249
	v_exp_f32_e32 v250, v250
	v_exp_f32_e32 v251, v251
	v_exp_f32_e32 v252, v252
	v_exp_f32_e32 v253, v253
	v_pk_add_f32 v[238:239], v[238:239], 1.0 op_sel_hi:[1,0]
	v_pk_add_f32 v[240:241], v[240:241], 1.0 op_sel_hi:[1,0]
	v_pk_add_f32 v[242:243], v[242:243], 1.0 op_sel_hi:[1,0]
	v_pk_add_f32 v[244:245], v[244:245], 1.0 op_sel_hi:[1,0]
	v_pk_add_f32 v[246:247], v[246:247], 1.0 op_sel_hi:[1,0]
	v_pk_add_f32 v[248:249], v[248:249], 1.0 op_sel_hi:[1,0]
	v_pk_add_f32 v[250:251], v[250:251], 1.0 op_sel_hi:[1,0]
	v_pk_add_f32 v[252:253], v[252:253], 1.0 op_sel_hi:[1,0]
	v_rcp_f32_e32 v238, v238
	v_rcp_f32_e32 v239, v239
	v_rcp_f32_e32 v240, v240
	v_rcp_f32_e32 v241, v241
	v_rcp_f32_e32 v242, v242
	v_rcp_f32_e32 v243, v243
	v_rcp_f32_e32 v244, v244
	v_rcp_f32_e32 v245, v245
	v_rcp_f32_e32 v246, v246
	v_rcp_f32_e32 v247, v247
	v_rcp_f32_e32 v248, v248
	v_rcp_f32_e32 v249, v249
	v_rcp_f32_e32 v250, v250
	v_rcp_f32_e32 v251, v251
	v_rcp_f32_e32 v252, v252
	v_rcp_f32_e32 v253, v253
	v_pk_mul_f32 v[238:239], v[126:127], v[238:239]
	v_pk_mul_f32 v[240:241], v[128:129], v[240:241]
	v_pk_mul_f32 v[242:243], v[118:119], v[242:243]
	v_pk_mul_f32 v[244:245], v[120:121], v[244:245]
	v_pk_mul_f32 v[246:247], v[110:111], v[246:247]
	v_pk_mul_f32 v[248:249], v[112:113], v[248:249]
	v_pk_mul_f32 v[250:251], v[102:103], v[250:251]
	v_pk_mul_f32 v[252:253], v[104:105], v[252:253]
	v_pk_mul_f32 v[122:123], v[122:123], v[238:239]
	v_pk_mul_f32 v[124:125], v[124:125], v[240:241]
	v_pk_mul_f32 v[114:115], v[114:115], v[242:243]
	v_pk_mul_f32 v[116:117], v[116:117], v[244:245]
	v_pk_mul_f32 v[106:107], v[106:107], v[246:247]
	v_pk_mul_f32 v[108:109], v[108:109], v[248:249]
	v_pk_mul_f32 v[98:99], v[98:99], v[250:251]
	v_pk_mul_f32 v[100:101], v[100:101], v[252:253]
	v_med3_f32 v122, v122, s78, v196
	v_med3_f32 v123, v123, s78, v196
	v_med3_f32 v124, v124, s78, v196
	v_med3_f32 v125, v125, s78, v196
	v_med3_f32 v114, v114, s78, v196
	v_med3_f32 v115, v115, s78, v196
	v_med3_f32 v116, v116, s78, v196
	v_med3_f32 v117, v117, s78, v196
	v_med3_f32 v106, v106, s78, v196
	v_med3_f32 v107, v107, s78, v196
	v_med3_f32 v108, v108, s78, v196
	v_med3_f32 v109, v109, s78, v196
	v_med3_f32 v98, v98, s78, v196
	v_med3_f32 v99, v99, s78, v196
	v_med3_f32 v100, v100, s78, v196
	v_med3_f32 v101, v101, s78, v196
	v_cvt_pk_fp8_f32 v158, v122, v123
	v_cvt_pk_fp8_f32 v159, v114, v115
	v_cvt_pk_fp8_f32 v160, v106, v107
	v_cvt_pk_fp8_f32 v161, v98, v99
	v_add_u32_e32 v197, 0x2c000, v211
	v_add_u32_e32 v26, 0x42000, v211
	v_cvt_pk_fp8_f32 v158, v124, v125 op_sel:[0,0,1]
	v_cvt_pk_fp8_f32 v159, v116, v117 op_sel:[0,0,1]
	v_cvt_pk_fp8_f32 v160, v108, v109 op_sel:[0,0,1]
	v_cvt_pk_fp8_f32 v161, v100, v101 op_sel:[0,0,1]
	s_nop 1
	global_store_dwordx2 v197, v[158:159], s[100:101]
	global_store_dwordx2 v26, v[160:161], s[100:101]
	v_mul_f32_e32 v30, 0x39000000, v22
	v_mul_f32_e32 v32, 0x39000000, v23
	v_mul_f32_e32 v31, 0x41000000, v30
	v_mul_f32_e32 v33, 0x41000000, v32
	v_pk_fma_f32 v[94:95], v[94:95], v[30:31], v[6:7] op_sel_hi:[1,0,1]
	v_pk_fma_f32 v[96:97], v[96:97], v[30:31], v[8:9] op_sel_hi:[1,0,1]
	v_pk_fma_f32 v[86:87], v[86:87], v[30:31], v[2:3] op_sel_hi:[1,0,1]
	v_pk_fma_f32 v[88:89], v[88:89], v[30:31], v[4:5] op_sel_hi:[1,0,1]
	v_pk_fma_f32 v[90:91], v[90:91], v[30:31], v[14:15] op_sel:[0,1,0] op_sel_hi:[1,1,1]
	v_pk_fma_f32 v[92:93], v[92:93], v[30:31], v[16:17] op_sel:[0,1,0] op_sel_hi:[1,1,1]
	v_pk_fma_f32 v[82:83], v[82:83], v[30:31], v[10:11] op_sel:[0,1,0] op_sel_hi:[1,1,1]
	v_pk_fma_f32 v[84:85], v[84:85], v[30:31], v[12:13] op_sel:[0,1,0] op_sel_hi:[1,1,1]
	v_pk_fma_f32 v[78:79], v[78:79], v[32:33], v[6:7] op_sel_hi:[1,0,1]
	v_pk_fma_f32 v[80:81], v[80:81], v[32:33], v[8:9] op_sel_hi:[1,0,1]
	v_pk_fma_f32 v[70:71], v[70:71], v[32:33], v[2:3] op_sel_hi:[1,0,1]
	v_pk_fma_f32 v[72:73], v[72:73], v[32:33], v[4:5] op_sel_hi:[1,0,1]
	v_pk_fma_f32 v[74:75], v[74:75], v[32:33], v[14:15] op_sel:[0,1,0] op_sel_hi:[1,1,1]
	v_pk_fma_f32 v[76:77], v[76:77], v[32:33], v[16:17] op_sel:[0,1,0] op_sel_hi:[1,1,1]
	v_pk_fma_f32 v[66:67], v[66:67], v[32:33], v[10:11] op_sel:[0,1,0] op_sel_hi:[1,1,1]
	v_pk_fma_f32 v[68:69], v[68:69], v[32:33], v[12:13] op_sel:[0,1,0] op_sel_hi:[1,1,1]
	v_pk_mul_f32 v[238:239], v[94:95], s[98:99] op_sel_hi:[1,0]
	v_pk_mul_f32 v[240:241], v[96:97], s[98:99] op_sel_hi:[1,0]
	v_pk_mul_f32 v[242:243], v[86:87], s[98:99] op_sel_hi:[1,0]
	v_pk_mul_f32 v[244:245], v[88:89], s[98:99] op_sel_hi:[1,0]
	v_pk_mul_f32 v[246:247], v[78:79], s[98:99] op_sel_hi:[1,0]
	v_pk_mul_f32 v[248:249], v[80:81], s[98:99] op_sel_hi:[1,0]
	v_pk_mul_f32 v[250:251], v[70:71], s[98:99] op_sel_hi:[1,0]
	v_pk_mul_f32 v[252:253], v[72:73], s[98:99] op_sel_hi:[1,0]
	v_exp_f32_e32 v238, v238
	v_exp_f32_e32 v239, v239
	v_exp_f32_e32 v240, v240
	v_exp_f32_e32 v241, v241
	v_exp_f32_e32 v242, v242
	v_exp_f32_e32 v243, v243
	v_exp_f32_e32 v244, v244
	v_exp_f32_e32 v245, v245
	v_exp_f32_e32 v246, v246
	v_exp_f32_e32 v247, v247
	v_exp_f32_e32 v248, v248
	v_exp_f32_e32 v249, v249
	v_exp_f32_e32 v250, v250
	v_exp_f32_e32 v251, v251
	v_exp_f32_e32 v252, v252
	v_exp_f32_e32 v253, v253
	v_pk_add_f32 v[238:239], v[238:239], 1.0 op_sel_hi:[1,0]
	v_pk_add_f32 v[240:241], v[240:241], 1.0 op_sel_hi:[1,0]
	v_pk_add_f32 v[242:243], v[242:243], 1.0 op_sel_hi:[1,0]
	v_pk_add_f32 v[244:245], v[244:245], 1.0 op_sel_hi:[1,0]
	v_pk_add_f32 v[246:247], v[246:247], 1.0 op_sel_hi:[1,0]
	v_pk_add_f32 v[248:249], v[248:249], 1.0 op_sel_hi:[1,0]
	v_pk_add_f32 v[250:251], v[250:251], 1.0 op_sel_hi:[1,0]
	v_pk_add_f32 v[252:253], v[252:253], 1.0 op_sel_hi:[1,0]
	v_rcp_f32_e32 v238, v238
	v_rcp_f32_e32 v239, v239
	v_rcp_f32_e32 v240, v240
	v_rcp_f32_e32 v241, v241
	v_rcp_f32_e32 v242, v242
	v_rcp_f32_e32 v243, v243
	v_rcp_f32_e32 v244, v244
	v_rcp_f32_e32 v245, v245
	v_rcp_f32_e32 v246, v246
	v_rcp_f32_e32 v247, v247
	v_rcp_f32_e32 v248, v248
	v_rcp_f32_e32 v249, v249
	v_rcp_f32_e32 v250, v250
	v_rcp_f32_e32 v251, v251
	v_rcp_f32_e32 v252, v252
	v_rcp_f32_e32 v253, v253
	v_pk_mul_f32 v[238:239], v[94:95], v[238:239]
	v_pk_mul_f32 v[240:241], v[96:97], v[240:241]
	v_pk_mul_f32 v[242:243], v[86:87], v[242:243]
	v_pk_mul_f32 v[244:245], v[88:89], v[244:245]
	v_pk_mul_f32 v[246:247], v[78:79], v[246:247]
	v_pk_mul_f32 v[248:249], v[80:81], v[248:249]
	v_pk_mul_f32 v[250:251], v[70:71], v[250:251]
	v_pk_mul_f32 v[252:253], v[72:73], v[252:253]
	v_pk_mul_f32 v[90:91], v[90:91], v[238:239]
	v_pk_mul_f32 v[92:93], v[92:93], v[240:241]
	v_pk_mul_f32 v[82:83], v[82:83], v[242:243]
	v_pk_mul_f32 v[84:85], v[84:85], v[244:245]
	v_pk_mul_f32 v[74:75], v[74:75], v[246:247]
	v_pk_mul_f32 v[76:77], v[76:77], v[248:249]
	v_pk_mul_f32 v[66:67], v[66:67], v[250:251]
	v_pk_mul_f32 v[68:69], v[68:69], v[252:253]
	v_med3_f32 v90, v90, s78, v196
	v_med3_f32 v91, v91, s78, v196
	v_med3_f32 v92, v92, s78, v196
	v_med3_f32 v93, v93, s78, v196
	v_med3_f32 v82, v82, s78, v196
	v_med3_f32 v83, v83, s78, v196
	v_med3_f32 v84, v84, s78, v196
	v_med3_f32 v85, v85, s78, v196
	v_med3_f32 v74, v74, s78, v196
	v_med3_f32 v75, v75, s78, v196
	v_med3_f32 v76, v76, s78, v196
	v_med3_f32 v77, v77, s78, v196
	v_med3_f32 v66, v66, s78, v196
	v_med3_f32 v67, v67, s78, v196
	v_med3_f32 v68, v68, s78, v196
	v_med3_f32 v69, v69, s78, v196
	v_cvt_pk_fp8_f32 v206, v90, v91
	v_cvt_pk_fp8_f32 v207, v82, v83
	v_cvt_pk_fp8_f32 v208, v74, v75
	v_cvt_pk_fp8_f32 v209, v66, v67
	v_add_u32_e32 v197, 0xb0000, v211
	v_add_u32_e32 v26, 0xc6000, v211
	v_cvt_pk_fp8_f32 v206, v92, v93 op_sel:[0,0,1]
	v_cvt_pk_fp8_f32 v207, v84, v85 op_sel:[0,0,1]
	v_cvt_pk_fp8_f32 v208, v76, v77 op_sel:[0,0,1]
	v_cvt_pk_fp8_f32 v209, v68, v69 op_sel:[0,0,1]
	s_nop 1
	global_store_dwordx2 v197, v[206:207], s[100:101]
	global_store_dwordx2 v26, v[208:209], s[100:101]
	v_mul_f32_e32 v30, 0x39000000, v18
	v_mul_f32_e32 v32, 0x39000000, v19
	v_mul_f32_e32 v31, 0x41000000, v30
	v_mul_f32_e32 v33, 0x41000000, v32
	v_pk_fma_f32 v[62:63], v[62:63], v[30:31], v[6:7] op_sel_hi:[1,0,1]
	v_pk_fma_f32 v[64:65], v[64:65], v[30:31], v[8:9] op_sel_hi:[1,0,1]
	v_pk_fma_f32 v[54:55], v[54:55], v[30:31], v[2:3] op_sel_hi:[1,0,1]
	v_pk_fma_f32 v[56:57], v[56:57], v[30:31], v[4:5] op_sel_hi:[1,0,1]
	v_pk_fma_f32 v[58:59], v[58:59], v[30:31], v[14:15] op_sel:[0,1,0] op_sel_hi:[1,1,1]
	v_pk_fma_f32 v[60:61], v[60:61], v[30:31], v[16:17] op_sel:[0,1,0] op_sel_hi:[1,1,1]
	v_pk_fma_f32 v[50:51], v[50:51], v[30:31], v[10:11] op_sel:[0,1,0] op_sel_hi:[1,1,1]
	v_pk_fma_f32 v[52:53], v[52:53], v[30:31], v[12:13] op_sel:[0,1,0] op_sel_hi:[1,1,1]
	v_pk_fma_f32 v[46:47], v[46:47], v[32:33], v[6:7] op_sel_hi:[1,0,1]
	v_pk_fma_f32 v[48:49], v[48:49], v[32:33], v[8:9] op_sel_hi:[1,0,1]
	v_pk_fma_f32 v[38:39], v[38:39], v[32:33], v[2:3] op_sel_hi:[1,0,1]
	v_pk_fma_f32 v[40:41], v[40:41], v[32:33], v[4:5] op_sel_hi:[1,0,1]
	v_pk_fma_f32 v[42:43], v[42:43], v[32:33], v[14:15] op_sel:[0,1,0] op_sel_hi:[1,1,1]
	v_pk_fma_f32 v[44:45], v[44:45], v[32:33], v[16:17] op_sel:[0,1,0] op_sel_hi:[1,1,1]
	v_pk_fma_f32 v[34:35], v[34:35], v[32:33], v[10:11] op_sel:[0,1,0] op_sel_hi:[1,1,1]
	v_pk_fma_f32 v[36:37], v[36:37], v[32:33], v[12:13] op_sel:[0,1,0] op_sel_hi:[1,1,1]
	v_pk_mul_f32 v[238:239], v[62:63], s[98:99] op_sel_hi:[1,0]
	v_pk_mul_f32 v[240:241], v[64:65], s[98:99] op_sel_hi:[1,0]
	v_pk_mul_f32 v[242:243], v[54:55], s[98:99] op_sel_hi:[1,0]
	v_pk_mul_f32 v[244:245], v[56:57], s[98:99] op_sel_hi:[1,0]
	v_pk_mul_f32 v[246:247], v[46:47], s[98:99] op_sel_hi:[1,0]
	v_pk_mul_f32 v[248:249], v[48:49], s[98:99] op_sel_hi:[1,0]
	v_pk_mul_f32 v[250:251], v[38:39], s[98:99] op_sel_hi:[1,0]
	v_pk_mul_f32 v[252:253], v[40:41], s[98:99] op_sel_hi:[1,0]
	v_exp_f32_e32 v238, v238
	v_exp_f32_e32 v239, v239
	v_exp_f32_e32 v240, v240
	v_exp_f32_e32 v241, v241
	v_exp_f32_e32 v242, v242
	v_exp_f32_e32 v243, v243
	v_exp_f32_e32 v244, v244
	v_exp_f32_e32 v245, v245
	v_exp_f32_e32 v246, v246
	v_exp_f32_e32 v247, v247
	v_exp_f32_e32 v248, v248
	v_exp_f32_e32 v249, v249
	v_exp_f32_e32 v250, v250
	v_exp_f32_e32 v251, v251
	v_exp_f32_e32 v252, v252
	v_exp_f32_e32 v253, v253
	v_pk_add_f32 v[238:239], v[238:239], 1.0 op_sel_hi:[1,0]
	v_pk_add_f32 v[240:241], v[240:241], 1.0 op_sel_hi:[1,0]
	v_pk_add_f32 v[242:243], v[242:243], 1.0 op_sel_hi:[1,0]
	v_pk_add_f32 v[244:245], v[244:245], 1.0 op_sel_hi:[1,0]
	v_pk_add_f32 v[246:247], v[246:247], 1.0 op_sel_hi:[1,0]
	v_pk_add_f32 v[248:249], v[248:249], 1.0 op_sel_hi:[1,0]
	v_pk_add_f32 v[250:251], v[250:251], 1.0 op_sel_hi:[1,0]
	v_pk_add_f32 v[252:253], v[252:253], 1.0 op_sel_hi:[1,0]
	v_rcp_f32_e32 v238, v238
	v_rcp_f32_e32 v239, v239
	v_rcp_f32_e32 v240, v240
	v_rcp_f32_e32 v241, v241
	v_rcp_f32_e32 v242, v242
	v_rcp_f32_e32 v243, v243
	v_rcp_f32_e32 v244, v244
	v_rcp_f32_e32 v245, v245
	v_rcp_f32_e32 v246, v246
	v_rcp_f32_e32 v247, v247
	v_rcp_f32_e32 v248, v248
	v_rcp_f32_e32 v249, v249
	v_rcp_f32_e32 v250, v250
	v_rcp_f32_e32 v251, v251
	v_rcp_f32_e32 v252, v252
	v_rcp_f32_e32 v253, v253
	v_pk_mul_f32 v[238:239], v[62:63], v[238:239]
	v_pk_mul_f32 v[240:241], v[64:65], v[240:241]
	v_pk_mul_f32 v[242:243], v[54:55], v[242:243]
	v_pk_mul_f32 v[244:245], v[56:57], v[244:245]
	v_pk_mul_f32 v[246:247], v[46:47], v[246:247]
	v_pk_mul_f32 v[248:249], v[48:49], v[248:249]
	v_pk_mul_f32 v[250:251], v[38:39], v[250:251]
	v_pk_mul_f32 v[252:253], v[40:41], v[252:253]
	v_pk_mul_f32 v[58:59], v[58:59], v[238:239]
	v_pk_mul_f32 v[60:61], v[60:61], v[240:241]
	v_pk_mul_f32 v[50:51], v[50:51], v[242:243]
	v_pk_mul_f32 v[52:53], v[52:53], v[244:245]
	v_pk_mul_f32 v[42:43], v[42:43], v[246:247]
	v_pk_mul_f32 v[44:45], v[44:45], v[248:249]
	v_pk_mul_f32 v[34:35], v[34:35], v[250:251]
	v_pk_mul_f32 v[36:37], v[36:37], v[252:253]
	v_med3_f32 v58, v58, s78, v196
	v_med3_f32 v59, v59, s78, v196
	v_med3_f32 v60, v60, s78, v196
	v_med3_f32 v61, v61, s78, v196
	v_med3_f32 v50, v50, s78, v196
	v_med3_f32 v51, v51, s78, v196
	v_med3_f32 v52, v52, s78, v196
	v_med3_f32 v53, v53, s78, v196
	v_med3_f32 v42, v42, s78, v196
	v_med3_f32 v43, v43, s78, v196
	v_med3_f32 v44, v44, s78, v196
	v_med3_f32 v45, v45, s78, v196
	v_med3_f32 v34, v34, s78, v196
	v_med3_f32 v35, v35, s78, v196
	v_med3_f32 v36, v36, s78, v196
	v_med3_f32 v37, v37, s78, v196
	v_cvt_pk_fp8_f32 v158, v58, v59
	v_cvt_pk_fp8_f32 v159, v50, v51
	v_cvt_pk_fp8_f32 v160, v42, v43
	v_cvt_pk_fp8_f32 v161, v34, v35
	v_add_u32_e32 v197, 0xdc000, v211
	v_add_u32_e32 v26, 0xf2000, v211
	v_cvt_pk_fp8_f32 v158, v60, v61 op_sel:[0,0,1]
	v_cvt_pk_fp8_f32 v159, v52, v53 op_sel:[0,0,1]
	v_cvt_pk_fp8_f32 v160, v44, v45 op_sel:[0,0,1]
	v_cvt_pk_fp8_f32 v161, v36, v37 op_sel:[0,0,1]
	s_nop 1
	global_store_dwordx2 v197, v[158:159], s[100:101]
	global_store_dwordx2 v26, v[160:161], s[100:101]
	s_andn2_b64 vcc, exec, s[2:3]
	s_mov_b64 s[2:3], -1
	s_cbranch_vccnz .LBB0_1392
	s_andn2_b64 vcc, exec, s[12:13]
	s_cbranch_vccnz .LBB0_1391
	s_barrier
	s_branch .LBB0_1391

.LBB0_1830:
	s_add_u32 s12, s38, 0x3ac00000
	s_addc_u32 s13, s39, 0
	s_add_u32 s60, s38, 0xa4500000
	v_and_b32_e32 v163, 15, v2
	v_lshrrev_b32_e32 v164, 4, v8
	v_and_b32_e32 v8, 48, v2
	v_lshlrev_b32_e32 v2, 2, v2
	s_addc_u32 s61, s39, 0
	v_lshlrev_b32_e32 v11, 6, v163
	v_and_b32_e32 v2, 32, v2
	s_add_i32 s64, s52, 0x18000
	v_bitop3_b32 v2, v11, v2, v8 bitop3:0x36
	v_add_u32_e32 v8, 0x80, v10
	s_mov_b32 m0, s64
	s_add_i32 s65, s52, 0x1a000
	s_waitcnt vmcnt(2)
	s_barrier
	global_load_lds_dwordx4 v8, s[20:21]
	v_add_u32_e32 v8, s45, v8
	s_mov_b32 m0, s65
	v_add_u32_e32 v165, 0x80, v1
	s_add_i32 s66, s52, 0x8000
	global_load_lds_dwordx4 v8, s[20:21]
	v_add_u32_e32 v8, s94, v165
	s_mov_b32 m0, s66
	s_add_i32 s67, s52, 0xa000
	global_load_lds_dwordx4 v8, s[8:9]
	v_add_u32_e32 v8, s44, v8
	s_mov_b32 m0, s67
	s_add_i32 s68, s52, 0x1c000
	global_load_lds_dwordx4 v8, s[8:9]
	v_add_u32_e32 v8, 0x80, v9
	s_mov_b32 m0, s68
	s_add_i32 s69, s52, 0x1e000
	global_load_lds_dwordx4 v8, s[20:21]
	v_add_u32_e32 v8, s45, v8
	s_mov_b32 m0, s69
	s_and_b32 s23, s15, 3
	global_load_lds_dwordx4 v8, s[20:21]
	s_ashr_i32 s15, s14, 31
	s_lshr_b32 s15, s15, 26
	s_add_i32 s15, s14, s15
	s_lshl_b32 s63, s16, 6
	s_lshl_b32 s24, s16, 13
	s_lshl_b32 s16, s23, 12
	s_ashr_i32 s62, s15, 6
	s_lshl_b32 s25, s23, 5
	s_add_i32 s16, s16, 0
	s_cmp_gt_i32 s14, 63
	v_add_u32_e32 v8, 0, v2
	v_add_u32_e32 v2, s16, v2
	s_cselect_b64 s[16:17], -1, 0
	s_add_i32 s70, s62, -2
	s_cmpk_lt_u32 s5, 0x100
	v_mov_b32_e32 v147, 0
	v_add_u32_e32 v166, 0x10000, v2
	v_add_u32_e32 v167, 0x14000, v2
	v_add_u32_e32 v168, 0x18000, v2
	v_add_u32_e32 v169, 0x1c000, v2
	s_cselect_b64 s[18:19], -1, 0
	v_add_u32_e32 v170, 0x10400, v2
	v_add_u32_e32 v171, 0x10800, v2
	v_add_u32_e32 v172, 0x10c00, v2
	v_add_u32_e32 v173, 0x14400, v2
	v_add_u32_e32 v174, 0x14800, v2
	v_add_u32_e32 v175, 0x14c00, v2
	v_add_u32_e32 v176, 0x18400, v2
	v_add_u32_e32 v177, 0x18800, v2
	v_add_u32_e32 v178, 0x18c00, v2
	v_add_u32_e32 v179, 0x1c400, v2
	v_add_u32_e32 v180, 0x1c800, v2
	v_add_u32_e32 v181, 0x1cc00, v2
	v_lshl_add_u64 v[148:149], s[2:3], 0, v[146:147]
	s_lshl_b32 s2, s23, 7
	v_lshlrev_b32_e32 v2, 4, v3
	s_add_i32 s74, s2, 0
	v_and_b32_e32 v2, 0xffffffe0, v2
	v_lshlrev_b32_e32 v5, 1, v5
	s_movk_i32 s2, 0x180
	v_add3_u32 v2, v2, v5, s2
	v_and_b32_e32 v3, 1, v3
	v_mul_lo_u32 v2, s4, v2
	v_lshlrev_b32_e32 v3, 6, v3
	v_lshlrev_b32_e32 v5, 1, v6
	s_waitcnt vmcnt(6)
	s_and_b32 s5, s5, 0xffffff00
	v_add3_u32 v182, v2, v3, v5
	v_add3_u32 v2, v7, v4, v6
	s_mov_b32 s15, 0
	s_lshl_b32 s14, s23, 6
	s_add_i32 s76, s5, 0
	v_lshl_add_u32 v183, v2, 1, s22
	v_mbcnt_lo_u32_b32 v2, -1, 0
	s_or_b32 s71, s14, s5
	s_ashr_i32 s72, s63, 31
	s_ashr_i32 s73, s34, 31
	s_add_i32 s74, s74, 0x21400
	s_add_i32 s76, s76, 0x21000
	s_mov_b32 s85, -1
	v_mov_b64_e32 v[150:151], 0x7bc
	v_mov_b64_e32 v[152:153], 0x7bb
	v_add_u32_e32 v184, s24, v8
	v_mov_b32_e32 v185, 0x358637bd
	s_movk_i32 s77, 0x1e00
	s_lshl_b32 s14, s25, 1
	s_mov_b32 s78, 0x3c000
	s_mov_b64 s[22:23], 0x5a000
	s_mov_b32 s79, 0x5a000
	s_mov_b64 s[24:25], 0xf0000
	s_mov_b32 s80, 0xf0000
	s_mov_b64 s[28:29], 0x10e000
	s_mov_b32 s81, 0x10e000
	s_mov_b64 s[30:31], 0x12c000
	s_mov_b32 s82, 0x12c000
	s_mov_b64 s[46:47], 0x14a000
	s_mov_b32 s83, 0x14a000
	v_mbcnt_hi_u32_b32 v186, -1, v2
	s_mov_b32 s92, s15
	s_mov_b32 s84, s15
	s_barrier
	s_branch .LBB0_1833
.Lzs_7:
	v_mov_b64_e32 v[2:3], 0
	v_mov_b64_e32 v[4:5], 0
	v_mov_b64_e32 v[6:7], 0
	v_mov_b64_e32 v[8:9], 0
	v_mov_b64_e32 v[10:11], 0
	v_mov_b64_e32 v[12:13], 0
	v_mov_b64_e32 v[14:15], 0
	v_mov_b64_e32 v[16:17], 0
	v_mov_b64_e32 v[18:19], 0
	v_mov_b64_e32 v[20:21], 0
	v_mov_b64_e32 v[22:23], 0
	v_mov_b64_e32 v[24:25], 0
	v_mov_b64_e32 v[26:27], 0
	v_mov_b64_e32 v[28:29], 0
	v_mov_b64_e32 v[30:31], 0
	v_mov_b64_e32 v[32:33], 0
	v_mov_b64_e32 v[34:35], 0
	v_mov_b64_e32 v[36:37], 0
	v_mov_b64_e32 v[38:39], 0
	v_mov_b64_e32 v[40:41], 0
	v_mov_b64_e32 v[42:43], 0
	v_mov_b64_e32 v[44:45], 0
	v_mov_b64_e32 v[46:47], 0
	v_mov_b64_e32 v[48:49], 0
	v_mov_b64_e32 v[50:51], 0
	v_mov_b64_e32 v[52:53], 0
	v_mov_b64_e32 v[54:55], 0
	v_mov_b64_e32 v[56:57], 0
	v_mov_b64_e32 v[58:59], 0
	v_mov_b64_e32 v[60:61], 0
	v_mov_b64_e32 v[62:63], 0
	v_mov_b64_e32 v[64:65], 0
	v_mov_b64_e32 v[66:67], 0
	v_mov_b64_e32 v[68:69], 0
	v_mov_b64_e32 v[70:71], 0
	v_mov_b64_e32 v[72:73], 0
	v_mov_b64_e32 v[74:75], 0
	v_mov_b64_e32 v[76:77], 0
	v_mov_b64_e32 v[78:79], 0
	v_mov_b64_e32 v[80:81], 0
	v_mov_b64_e32 v[82:83], 0
	v_mov_b64_e32 v[84:85], 0
	v_mov_b64_e32 v[86:87], 0
	v_mov_b64_e32 v[88:89], 0
	v_mov_b64_e32 v[90:91], 0
	v_mov_b64_e32 v[92:93], 0
	v_mov_b64_e32 v[94:95], 0
	v_mov_b64_e32 v[96:97], 0
	v_mov_b64_e32 v[98:99], 0
	v_mov_b64_e32 v[100:101], 0
	v_mov_b64_e32 v[102:103], 0
	v_mov_b64_e32 v[104:105], 0
	v_mov_b64_e32 v[106:107], 0
	v_mov_b64_e32 v[108:109], 0
	v_mov_b64_e32 v[110:111], 0
	v_mov_b64_e32 v[112:113], 0
	v_mov_b64_e32 v[114:115], 0
	v_mov_b64_e32 v[116:117], 0
	v_mov_b64_e32 v[118:119], 0
	v_mov_b64_e32 v[120:121], 0
	v_mov_b64_e32 v[122:123], 0
	v_mov_b64_e32 v[124:125], 0
	v_mov_b64_e32 v[126:127], 0
	v_mov_b64_e32 v[128:129], 0
	s_branch .LBB0_1844

.LBB0_1839:
	s_and_b32 s90, s84, 1
	s_andn2_b64 vcc, exec, s[16:17]
	s_cbranch_vccnz .Lzs_7
	s_min_i32 s50, s89, 0x80
	s_lshr_b32 s75, s50, 5
	s_lshl_b32 s50, s86, 8
	s_ashr_i32 s51, s50, 31
	v_lshl_add_u64 v[2:3], s[50:51], 2, v[148:149]
	s_mul_i32 s50, s75, 0xf00
	s_lshl_b32 s97, s90, 10
	s_ashr_i32 s51, s50, 31
	v_lshl_add_u64 v[130:131], s[50:51], 2, v[2:3]
	s_add_i32 s97, s97, 0
	s_or_b64 s[4:5], s[6:7], s[4:5]
	s_addk_i32 s94, 0x80
	s_addk_i32 s95, 0x100
	s_mov_b32 s96, 0
	s_add_i32 s97, s97, 0x21400
	v_mov_b64_e32 v[2:3], 0
	v_mov_b64_e32 v[4:5], 0
	v_mov_b64_e32 v[6:7], 0
	v_mov_b64_e32 v[8:9], 0
	v_mov_b64_e32 v[10:11], 0
	v_mov_b64_e32 v[12:13], 0
	v_mov_b64_e32 v[14:15], 0
	v_mov_b64_e32 v[16:17], 0
	v_mov_b64_e32 v[18:19], 0
	v_mov_b64_e32 v[20:21], 0
	v_mov_b64_e32 v[22:23], 0
	v_mov_b64_e32 v[24:25], 0
	v_mov_b64_e32 v[26:27], 0
	v_mov_b64_e32 v[28:29], 0
	v_mov_b64_e32 v[30:31], 0
	v_mov_b64_e32 v[32:33], 0
	v_mov_b64_e32 v[34:35], 0
	v_mov_b64_e32 v[36:37], 0
	v_mov_b64_e32 v[38:39], 0
	v_mov_b64_e32 v[40:41], 0
	v_mov_b64_e32 v[42:43], 0
	v_mov_b64_e32 v[44:45], 0
	v_mov_b64_e32 v[46:47], 0
	v_mov_b64_e32 v[48:49], 0
	v_mov_b64_e32 v[50:51], 0
	v_mov_b64_e32 v[52:53], 0
	v_mov_b64_e32 v[54:55], 0
	v_mov_b64_e32 v[56:57], 0
	v_mov_b64_e32 v[58:59], 0
	v_mov_b64_e32 v[60:61], 0
	v_mov_b64_e32 v[62:63], 0
	v_mov_b64_e32 v[64:65], 0
	v_mov_b64_e32 v[66:67], 0
	v_mov_b64_e32 v[68:69], 0
	v_mov_b64_e32 v[70:71], 0
	v_mov_b64_e32 v[72:73], 0
	v_mov_b64_e32 v[74:75], 0
	v_mov_b64_e32 v[76:77], 0
	v_mov_b64_e32 v[78:79], 0
	v_mov_b64_e32 v[80:81], 0
	v_mov_b64_e32 v[82:83], 0
	v_mov_b64_e32 v[84:85], 0
	v_mov_b64_e32 v[86:87], 0
	v_mov_b64_e32 v[88:89], 0
	v_mov_b64_e32 v[90:91], 0
	v_mov_b64_e32 v[92:93], 0
	v_mov_b64_e32 v[94:95], 0
	v_mov_b64_e32 v[96:97], 0
	v_mov_b64_e32 v[98:99], 0
	v_mov_b64_e32 v[100:101], 0
	v_mov_b64_e32 v[102:103], 0
	v_mov_b64_e32 v[104:105], 0
	v_mov_b64_e32 v[106:107], 0
	v_mov_b64_e32 v[108:109], 0
	v_mov_b64_e32 v[110:111], 0
	v_mov_b64_e32 v[112:113], 0
	v_mov_b64_e32 v[114:115], 0
	v_mov_b64_e32 v[116:117], 0
	v_mov_b64_e32 v[118:119], 0
	v_mov_b64_e32 v[120:121], 0
	v_mov_b64_e32 v[122:123], 0
	v_mov_b64_e32 v[124:125], 0
	v_mov_b64_e32 v[126:127], 0
	v_mov_b64_e32 v[128:129], 0
	s_branch .LBB0_1842

.LBB0_2926:
	s_add_u32 s12, s38, 0x4b400000
	v_mov_b32_e32 v3, v177
	s_addc_u32 s13, s39, 0
	s_waitcnt vmcnt(2)
	s_barrier
	s_or_b32 s18, s83, 0x80
	s_add_i32 s58, s49, 0x18000
	s_mov_b32 m0, s58
	v_add_u32_e32 v3, s18, v3
	global_load_lds_dwordx4 v3, s[6:7]
	v_mov_b32_e32 v3, v177
	s_add_i32 s18, s18, s48
	s_add_i32 s59, s49, 0x1a000
	v_add_u32_e32 v3, s18, v3
	s_mov_b32 m0, s59
	s_or_b32 s18, s82, 0x80
	global_load_lds_dwordx4 v3, s[6:7]
	v_mov_b32_e32 v3, v176
	s_add_i32 s60, s49, 0x8000
	v_add_u32_e32 v3, s18, v3
	s_mov_b32 m0, s60
	s_add_i32 s18, s18, s47
	global_load_lds_dwordx4 v3, s[4:5]
	v_mov_b32_e32 v3, v176
	s_add_i32 s61, s49, 0xa000
	s_lshl_b32 s17, s17, 8
	v_add_u32_e32 v3, s18, v3
	s_mov_b32 m0, s61
	s_add_i32 s17, s83, s17
	global_load_lds_dwordx4 v3, s[4:5]
	v_mov_b32_e32 v3, v177
	s_addk_i32 s17, 0x80
	s_add_i32 s62, s49, 0x1c000
	s_mov_b32 m0, s62
	v_add_u32_e32 v3, s17, v3
	global_load_lds_dwordx4 v3, s[6:7]
	v_mov_b32_e32 v3, v177
	s_add_i32 s17, s17, s48
	s_add_i32 s63, s49, 0x1e000
	v_add_u32_e32 v3, s17, v3
	s_mov_b32 m0, s63
	s_ashr_i32 s17, s14, 31
	global_load_lds_dwordx4 v3, s[6:7]
	s_and_b32 s15, s15, 3
	s_lshr_b32 s17, s17, 26
	v_and_b32_e32 v178, 15, v2
	v_bfe_u32 v179, v2, 4, 2
	s_add_i32 s17, s14, s17
	s_lshl_b32 s66, s8, 6
	v_and_b32_e32 v3, 48, v2
	s_lshl_b32 s18, s8, 13
	s_lshl_b32 s8, s15, 5
	s_lshl_b32 s15, s15, 12
	v_lshlrev_b32_e32 v2, 2, v2
	s_ashr_i32 s64, s17, 6
	s_lshl_b32 s65, s70, 8
	v_lshlrev_b32_e32 v4, 6, v178
	v_and_b32_e32 v2, 32, v2
	s_add_i32 s15, s15, 0
	v_bitop3_b32 v2, v4, v2, v3 bitop3:0x36
	s_cmp_gt_i32 s14, 63
	v_add_u32_e32 v3, 0, v2
	v_add_u32_e32 v2, s15, v2
	s_waitcnt vmcnt(6)
	s_cselect_b64 s[14:15], -1, 0
	s_add_i32 s67, s64, -2
	s_cmpk_lt_u32 s16, 0x100
	v_add_u32_e32 v180, 0x10000, v2
	v_add_u32_e32 v181, 0x10400, v2
	v_add_u32_e32 v182, 0x14000, v2
	v_add_u32_e32 v183, 0x14400, v2
	v_add_u32_e32 v184, 0x18000, v2
	v_add_u32_e32 v185, 0x18400, v2
	v_add_u32_e32 v186, 0x1c000, v2
	v_add_u32_e32 v187, 0x1c400, v2
	s_cselect_b64 s[16:17], -1, 0
	s_ashr_i32 s68, s66, 31
	v_add_u32_e32 v188, 0x10800, v2
	v_add_u32_e32 v189, 0x10c00, v2
	v_add_u32_e32 v190, 0x14800, v2
	v_add_u32_e32 v191, 0x14c00, v2
	v_add_u32_e32 v192, 0x18800, v2
	v_add_u32_e32 v193, 0x18c00, v2
	v_add_u32_e32 v194, 0x1c800, v2
	v_add_u32_e32 v195, 0x1cc00, v2
	s_ashr_i32 s69, s34, 31
	s_mulk_i32 s70, 0x180
	v_mov_b64_e32 v[162:163], s[2:3]
	v_add_u32_e32 v196, s18, v3
	s_mov_b32 s18, 0x39000000
	s_mov_b32 s20, 0x3a800000
	s_movk_i32 s71, 0x1600
	s_mov_b32 s72, 0xc3e00000
	s_mov_b32 s73, 0x2c000
	s_mov_b32 s74, 0x42000
	s_mov_b32 s75, 0xb0000
	s_mov_b32 s76, 0xc6000
	s_mov_b32 s77, 0xdc000
	v_mov_b32_e32 v197, 0x43e00000
	s_mov_b32 s78, s9
	s_barrier
	s_branch .LBB0_2929
.Lzs_12:
	v_mov_b64_e32 v[34:35], 0
	v_mov_b64_e32 v[36:37], 0
	v_mov_b64_e32 v[38:39], 0
	v_mov_b64_e32 v[40:41], 0
	v_mov_b64_e32 v[42:43], 0
	v_mov_b64_e32 v[44:45], 0
	v_mov_b64_e32 v[46:47], 0
	v_mov_b64_e32 v[48:49], 0
	v_mov_b64_e32 v[50:51], 0
	v_mov_b64_e32 v[52:53], 0
	v_mov_b64_e32 v[54:55], 0
	v_mov_b64_e32 v[56:57], 0
	v_mov_b64_e32 v[58:59], 0
	v_mov_b64_e32 v[60:61], 0
	v_mov_b64_e32 v[62:63], 0
	v_mov_b64_e32 v[64:65], 0
	v_mov_b64_e32 v[66:67], 0
	v_mov_b64_e32 v[68:69], 0
	v_mov_b64_e32 v[70:71], 0
	v_mov_b64_e32 v[72:73], 0
	v_mov_b64_e32 v[74:75], 0
	v_mov_b64_e32 v[76:77], 0
	v_mov_b64_e32 v[78:79], 0
	v_mov_b64_e32 v[80:81], 0
	v_mov_b64_e32 v[82:83], 0
	v_mov_b64_e32 v[84:85], 0
	v_mov_b64_e32 v[86:87], 0
	v_mov_b64_e32 v[88:89], 0
	v_mov_b64_e32 v[90:91], 0
	v_mov_b64_e32 v[92:93], 0
	v_mov_b64_e32 v[94:95], 0
	v_mov_b64_e32 v[96:97], 0
	v_mov_b64_e32 v[98:99], 0
	v_mov_b64_e32 v[100:101], 0
	v_mov_b64_e32 v[102:103], 0
	v_mov_b64_e32 v[104:105], 0
	v_mov_b64_e32 v[106:107], 0
	v_mov_b64_e32 v[108:109], 0
	v_mov_b64_e32 v[110:111], 0
	v_mov_b64_e32 v[112:113], 0
	v_mov_b64_e32 v[114:115], 0
	v_mov_b64_e32 v[116:117], 0
	v_mov_b64_e32 v[118:119], 0
	v_mov_b64_e32 v[120:121], 0
	v_mov_b64_e32 v[122:123], 0
	v_mov_b64_e32 v[124:125], 0
	v_mov_b64_e32 v[126:127], 0
	v_mov_b64_e32 v[128:129], 0
	v_mov_b64_e32 v[130:131], 0
	v_mov_b64_e32 v[132:133], 0
	v_mov_b64_e32 v[134:135], 0
	v_mov_b64_e32 v[136:137], 0
	v_mov_b64_e32 v[138:139], 0
	v_mov_b64_e32 v[140:141], 0
	v_mov_b64_e32 v[142:143], 0
	v_mov_b64_e32 v[144:145], 0
	v_mov_b64_e32 v[146:147], 0
	v_mov_b64_e32 v[148:149], 0
	v_mov_b64_e32 v[150:151], 0
	v_mov_b64_e32 v[152:153], 0
	v_mov_b64_e32 v[154:155], 0
	v_mov_b64_e32 v[156:157], 0
	v_mov_b64_e32 v[158:159], 0
	v_mov_b64_e32 v[160:161], 0
	s_branch .LBB0_2939

.Ltx23_skip:
	ds_read_b128 v[2:5], v184
	ds_read_b128 v[6:9], v185
	ds_read_b128 v[10:13], v192
	ds_read_b128 v[14:17], v193
	ds_read_b128 v[18:21], v186
	ds_read_b128 v[22:25], v187
	ds_read_b128 v[26:29], v194
	ds_read_b128 v[30:33], v195
	v_mov_b32_e32 v172, v176
	ds_read_b128 v[164:167], v196 offset:32768
	ds_read_b128 v[168:171], v196 offset:33792
	ds_read_b128 v[198:201], v196 offset:34816
	ds_read_b128 v[202:205], v196 offset:35840
	ds_read_b128 v[214:217], v196 offset:36864
	ds_read_b128 v[218:221], v196 offset:37888
	ds_read_b128 v[222:225], v196 offset:38912
	ds_read_b128 v[226:229], v196 offset:39936
	s_add_i32 s86, s86, s47
	s_mov_b32 m0, s55
	v_add_u32_e32 v172, s86, v172
	global_load_lds_dwordx4 v172, s[4:5]
	v_mov_b32_e32 v172, v176
	s_add_i32 s86, s86, s47
	v_add_u32_e32 v172, s86, v172
	s_mov_b32 m0, s56
	s_nop 0
	global_load_lds_dwordx4 v172, s[4:5]
	s_waitcnt vmcnt(8)
	s_waitcnt lgkmcnt(0)
	s_barrier
	s_setprio 1
	s_waitcnt lgkmcnt(0)
	v_mfma_f32_16x16x128_f8f6f4 v[158:161], v[2:9], v[164:171], v[158:161]
	v_mfma_f32_16x16x128_f8f6f4 v[154:157], v[10:17], v[164:171], v[154:157]
	v_mfma_f32_16x16x128_f8f6f4 v[150:153], v[2:9], v[198:205], v[150:153]
	v_mfma_f32_16x16x128_f8f6f4 v[146:149], v[10:17], v[198:205], v[146:149]
	v_mfma_f32_16x16x128_f8f6f4 v[138:141], v[2:9], v[214:221], v[138:141]
	v_mfma_f32_16x16x128_f8f6f4 v[130:133], v[10:17], v[214:221], v[130:133]
	v_mfma_f32_16x16x128_f8f6f4 v[122:125], v[2:9], v[222:229], v[122:125]
	v_mfma_f32_16x16x128_f8f6f4 v[114:117], v[10:17], v[222:229], v[114:117]
	s_setprio 0
	s_setprio 1
	v_mfma_f32_16x16x128_f8f6f4 v[142:145], v[18:25], v[164:171], v[142:145]
	v_mfma_f32_16x16x128_f8f6f4 v[134:137], v[26:33], v[164:171], v[134:137]
	v_mfma_f32_16x16x128_f8f6f4 v[126:129], v[18:25], v[198:205], v[126:129]
	v_mfma_f32_16x16x128_f8f6f4 v[118:121], v[26:33], v[198:205], v[118:121]
	v_mfma_f32_16x16x128_f8f6f4 v[110:113], v[18:25], v[214:221], v[110:113]
	v_mfma_f32_16x16x128_f8f6f4 v[106:109], v[26:33], v[214:221], v[106:109]
	v_mfma_f32_16x16x128_f8f6f4 v[102:105], v[18:25], v[222:229], v[102:105]
	v_mfma_f32_16x16x128_f8f6f4 v[98:101], v[26:33], v[222:229], v[98:101]
	s_setprio 0
	s_barrier
	v_mov_b32_e32 v172, v177
	ds_read_b128 v[164:167], v196 offset:49152
	ds_read_b128 v[168:171], v196 offset:50176
	ds_read_b128 v[198:201], v196 offset:51200
	ds_read_b128 v[202:205], v196 offset:52224
	ds_read_b128 v[214:217], v196 offset:53248
	ds_read_b128 v[218:221], v196 offset:54272
	ds_read_b128 v[222:225], v196 offset:55296
	ds_read_b128 v[226:229], v196 offset:56320
	s_mov_b32 m0, s58
	v_add_u32_e32 v172, s85, v172
	global_load_lds_dwordx4 v172, s[6:7]
	v_mov_b32_e32 v172, v177
	s_add_i32 s85, s85, s48
	v_add_u32_e32 v172, s85, v172
	s_mov_b32 m0, s59
	s_add_i32 s85, s85, s48
	global_load_lds_dwordx4 v172, s[6:7]
	v_mov_b32_e32 v172, v177
	s_mov_b32 m0, s62
	v_add_u32_e32 v172, s85, v172
	global_load_lds_dwordx4 v172, s[6:7]
	v_mov_b32_e32 v172, v177
	s_add_i32 s85, s85, s48
	v_add_u32_e32 v172, s85, v172
	s_mov_b32 m0, s63
	s_nop 0
	global_load_lds_dwordx4 v172, s[6:7]
	v_mov_b32_e32 v172, v176
	s_mov_b32 m0, s60
	v_add_u32_e32 v172, s84, v172
	global_load_lds_dwordx4 v172, s[4:5]
	v_mov_b32_e32 v172, v176
	s_add_i32 s84, s84, s47
	v_add_u32_e32 v172, s84, v172
	s_mov_b32 m0, s61
	s_nop 0
	global_load_lds_dwordx4 v172, s[4:5]
	s_waitcnt vmcnt(8)
	s_waitcnt lgkmcnt(0)
	s_barrier
	s_setprio 1
	s_waitcnt lgkmcnt(0)
	v_mfma_f32_16x16x128_f8f6f4 v[94:97], v[2:9], v[164:171], v[94:97]
	v_mfma_f32_16x16x128_f8f6f4 v[90:93], v[10:17], v[164:171], v[90:93]
	v_mfma_f32_16x16x128_f8f6f4 v[86:89], v[2:9], v[198:205], v[86:89]
	v_mfma_f32_16x16x128_f8f6f4 v[82:85], v[10:17], v[198:205], v[82:85]
	v_mfma_f32_16x16x128_f8f6f4 v[74:77], v[2:9], v[214:221], v[74:77]
	v_mfma_f32_16x16x128_f8f6f4 v[66:69], v[10:17], v[214:221], v[66:69]
	v_mfma_f32_16x16x128_f8f6f4 v[58:61], v[2:9], v[222:229], v[58:61]
	v_mfma_f32_16x16x128_f8f6f4 v[50:53], v[10:17], v[222:229], v[50:53]
	s_setprio 0
	s_setprio 1
	v_mfma_f32_16x16x128_f8f6f4 v[78:81], v[18:25], v[164:171], v[78:81]
	v_mfma_f32_16x16x128_f8f6f4 v[70:73], v[26:33], v[164:171], v[70:73]
	v_mfma_f32_16x16x128_f8f6f4 v[62:65], v[18:25], v[198:205], v[62:65]
	v_mfma_f32_16x16x128_f8f6f4 v[54:57], v[26:33], v[198:205], v[54:57]
	v_mfma_f32_16x16x128_f8f6f4 v[46:49], v[18:25], v[214:221], v[46:49]
	v_mfma_f32_16x16x128_f8f6f4 v[42:45], v[26:33], v[214:221], v[42:45]
	v_mfma_f32_16x16x128_f8f6f4 v[38:41], v[18:25], v[222:229], v[38:41]
	v_mfma_f32_16x16x128_f8f6f4 v[34:37], v[26:33], v[222:229], v[34:37]
	s_setprio 0
	s_barrier
	s_add_i32 s83, s83, 2
	s_addk_i32 s28, 0x100
	s_addk_i32 s82, 0x100
	s_cmp_ge_i32 s83, s64
	s_cbranch_scc0 .LBB0_2937
.LBB0_2939:
	s_and_b64 vcc, exec, s[16:17]
	s_cbranch_vccz .LBB0_2941
	s_barrier
.LBB0_2941:
	s_nop 15
	s_nop 15
	s_mul_hi_i32 s25, s81, 0x2e8ba2e9
	s_lshr_b32 s28, s25, 31
	s_lshr_b32 s25, s25, 3
	s_add_i32 s25, s25, s28
	s_mul_i32 s25, s25, 44
	s_sub_i32 s25, s81, s25
	s_lshl_b32 s28, s25, 7
	s_lshl_b32 s24, s24, 8
	s_add_i32 s24, s24, s66
	s_mul_i32 s24, s24, s71
	s_add_i32 s24, s24, s28
	s_add_i32 s24, s24, s8
	s_add_u32 s100, s12, s24
	s_addc_u32 s101, s13, 0
	s_mov_b32 s98, 0xbfb8aa3b
	v_mul_u32_u24_e32 v206, s71, v178
	v_lshl_add_u32 v206, v179, 3, v206
	v_pk_fma_f32 v[158:159], v[158:159], s[18:19], 0 op_sel_hi:[1,0,0]
	v_pk_fma_f32 v[160:161], v[160:161], s[18:19], 0 op_sel_hi:[1,0,0]
	v_pk_fma_f32 v[154:155], v[154:155], s[18:19], 0 op_sel_hi:[1,0,0]
	v_pk_fma_f32 v[156:157], v[156:157], s[18:19], 0 op_sel_hi:[1,0,0]
	v_pk_fma_f32 v[142:143], v[142:143], s[20:21], 0 op_sel_hi:[1,0,0]
	v_pk_fma_f32 v[144:145], v[144:145], s[20:21], 0 op_sel_hi:[1,0,0]
	v_pk_fma_f32 v[134:135], v[134:135], s[20:21], 0 op_sel_hi:[1,0,0]
	v_pk_fma_f32 v[136:137], v[136:137], s[20:21], 0 op_sel_hi:[1,0,0]
	v_pk_fma_f32 v[150:151], v[150:151], s[18:19], 0 op_sel_hi:[1,0,0]
	v_pk_fma_f32 v[152:153], v[152:153], s[18:19], 0 op_sel_hi:[1,0,0]
	v_pk_fma_f32 v[146:147], v[146:147], s[18:19], 0 op_sel_hi:[1,0,0]
	v_pk_fma_f32 v[148:149], v[148:149], s[18:19], 0 op_sel_hi:[1,0,0]
	v_pk_fma_f32 v[126:127], v[126:127], s[20:21], 0 op_sel_hi:[1,0,0]
	v_pk_fma_f32 v[128:129], v[128:129], s[20:21], 0 op_sel_hi:[1,0,0]
	v_pk_fma_f32 v[118:119], v[118:119], s[20:21], 0 op_sel_hi:[1,0,0]
	v_pk_fma_f32 v[120:121], v[120:121], s[20:21], 0 op_sel_hi:[1,0,0]
	v_pk_mul_f32 v[230:231], v[158:159], s[98:99] op_sel_hi:[1,0]
	v_pk_mul_f32 v[232:233], v[160:161], s[98:99] op_sel_hi:[1,0]
	v_pk_mul_f32 v[234:235], v[154:155], s[98:99] op_sel_hi:[1,0]
	v_pk_mul_f32 v[236:237], v[156:157], s[98:99] op_sel_hi:[1,0]
	v_pk_mul_f32 v[238:239], v[150:151], s[98:99] op_sel_hi:[1,0]
	v_pk_mul_f32 v[240:241], v[152:153], s[98:99] op_sel_hi:[1,0]
	v_pk_mul_f32 v[242:243], v[146:147], s[98:99] op_sel_hi:[1,0]
	v_pk_mul_f32 v[244:245], v[148:149], s[98:99] op_sel_hi:[1,0]
	v_exp_f32_e32 v230, v230
	v_exp_f32_e32 v231, v231
	v_exp_f32_e32 v232, v232
	v_exp_f32_e32 v233, v233
	v_exp_f32_e32 v234, v234
	v_exp_f32_e32 v235, v235
	v_exp_f32_e32 v236, v236
	v_exp_f32_e32 v237, v237
	v_exp_f32_e32 v238, v238
	v_exp_f32_e32 v239, v239
	v_exp_f32_e32 v240, v240
	v_exp_f32_e32 v241, v241
	v_exp_f32_e32 v242, v242
	v_exp_f32_e32 v243, v243
	v_exp_f32_e32 v244, v244
	v_exp_f32_e32 v245, v245
	v_pk_add_f32 v[230:231], v[230:231], 1.0 op_sel_hi:[1,0]
	v_pk_add_f32 v[232:233], v[232:233], 1.0 op_sel_hi:[1,0]
	v_pk_add_f32 v[234:235], v[234:235], 1.0 op_sel_hi:[1,0]
	v_pk_add_f32 v[236:237], v[236:237], 1.0 op_sel_hi:[1,0]
	v_pk_add_f32 v[238:239], v[238:239], 1.0 op_sel_hi:[1,0]
	v_pk_add_f32 v[240:241], v[240:241], 1.0 op_sel_hi:[1,0]
	v_pk_add_f32 v[242:243], v[242:243], 1.0 op_sel_hi:[1,0]
	v_pk_add_f32 v[244:245], v[244:245], 1.0 op_sel_hi:[1,0]
	v_rcp_f32_e32 v230, v230
	v_rcp_f32_e32 v231, v231
	v_rcp_f32_e32 v232, v232
	v_rcp_f32_e32 v233, v233
	v_rcp_f32_e32 v234, v234
	v_rcp_f32_e32 v235, v235
	v_rcp_f32_e32 v236, v236
	v_rcp_f32_e32 v237, v237
	v_rcp_f32_e32 v238, v238
	v_rcp_f32_e32 v239, v239
	v_rcp_f32_e32 v240, v240
	v_rcp_f32_e32 v241, v241
	v_rcp_f32_e32 v242, v242
	v_rcp_f32_e32 v243, v243
	v_rcp_f32_e32 v244, v244
	v_rcp_f32_e32 v245, v245
	v_pk_mul_f32 v[230:231], v[158:159], v[230:231]
	v_pk_mul_f32 v[232:233], v[160:161], v[232:233]
	v_pk_mul_f32 v[234:235], v[154:155], v[234:235]
	v_pk_mul_f32 v[236:237], v[156:157], v[236:237]
	v_pk_mul_f32 v[238:239], v[150:151], v[238:239]
	v_pk_mul_f32 v[240:241], v[152:153], v[240:241]
	v_pk_mul_f32 v[242:243], v[146:147], v[242:243]
	v_pk_mul_f32 v[244:245], v[148:149], v[244:245]
	v_pk_mul_f32 v[142:143], v[142:143], v[230:231]
	v_pk_mul_f32 v[144:145], v[144:145], v[232:233]
	v_pk_mul_f32 v[134:135], v[134:135], v[234:235]
	v_pk_mul_f32 v[136:137], v[136:137], v[236:237]
	v_pk_mul_f32 v[126:127], v[126:127], v[238:239]
	v_pk_mul_f32 v[128:129], v[128:129], v[240:241]
	v_pk_mul_f32 v[118:119], v[118:119], v[242:243]
	v_pk_mul_f32 v[120:121], v[120:121], v[244:245]
	v_med3_f32 v142, v142, s72, v197
	v_med3_f32 v143, v143, s72, v197
	v_med3_f32 v144, v144, s72, v197
	v_med3_f32 v145, v145, s72, v197
	v_med3_f32 v134, v134, s72, v197
	v_med3_f32 v135, v135, s72, v197
	v_med3_f32 v136, v136, s72, v197
	v_med3_f32 v137, v137, s72, v197
	v_med3_f32 v126, v126, s72, v197
	v_med3_f32 v127, v127, s72, v197
	v_med3_f32 v128, v128, s72, v197
	v_med3_f32 v129, v129, s72, v197
	v_med3_f32 v118, v118, s72, v197
	v_med3_f32 v119, v119, s72, v197
	v_med3_f32 v120, v120, s72, v197
	v_med3_f32 v121, v121, s72, v197
	v_cvt_pk_fp8_f32 v246, v142, v143
	v_cvt_pk_fp8_f32 v247, v134, v135
	v_cvt_pk_fp8_f32 v248, v126, v127
	v_cvt_pk_fp8_f32 v249, v118, v119
	v_add_u32_e32 v208, s57, v206
	v_cvt_pk_fp8_f32 v246, v144, v145 op_sel:[0,0,1]
	v_cvt_pk_fp8_f32 v247, v136, v137 op_sel:[0,0,1]
	v_cvt_pk_fp8_f32 v248, v128, v129 op_sel:[0,0,1]
	v_cvt_pk_fp8_f32 v249, v120, v121 op_sel:[0,0,1]
	s_nop 1
	global_store_dwordx2 v206, v[246:247], s[100:101]
	global_store_dwordx2 v208, v[248:249], s[100:101]
	v_pk_fma_f32 v[138:139], v[138:139], s[18:19], 0 op_sel_hi:[1,0,0]
	v_pk_fma_f32 v[140:141], v[140:141], s[18:19], 0 op_sel_hi:[1,0,0]
	v_pk_fma_f32 v[130:131], v[130:131], s[18:19], 0 op_sel_hi:[1,0,0]
	v_pk_fma_f32 v[132:133], v[132:133], s[18:19], 0 op_sel_hi:[1,0,0]
	v_pk_fma_f32 v[110:111], v[110:111], s[20:21], 0 op_sel_hi:[1,0,0]
	v_pk_fma_f32 v[112:113], v[112:113], s[20:21], 0 op_sel_hi:[1,0,0]
	v_pk_fma_f32 v[106:107], v[106:107], s[20:21], 0 op_sel_hi:[1,0,0]
	v_pk_fma_f32 v[108:109], v[108:109], s[20:21], 0 op_sel_hi:[1,0,0]
	v_pk_fma_f32 v[122:123], v[122:123], s[18:19], 0 op_sel_hi:[1,0,0]
	v_pk_fma_f32 v[124:125], v[124:125], s[18:19], 0 op_sel_hi:[1,0,0]
	v_pk_fma_f32 v[114:115], v[114:115], s[18:19], 0 op_sel_hi:[1,0,0]
	v_pk_fma_f32 v[116:117], v[116:117], s[18:19], 0 op_sel_hi:[1,0,0]
	v_pk_fma_f32 v[102:103], v[102:103], s[20:21], 0 op_sel_hi:[1,0,0]
	v_pk_fma_f32 v[104:105], v[104:105], s[20:21], 0 op_sel_hi:[1,0,0]
	v_pk_fma_f32 v[98:99], v[98:99], s[20:21], 0 op_sel_hi:[1,0,0]
	v_pk_fma_f32 v[100:101], v[100:101], s[20:21], 0 op_sel_hi:[1,0,0]
	v_pk_mul_f32 v[230:231], v[138:139], s[98:99] op_sel_hi:[1,0]
	v_pk_mul_f32 v[232:233], v[140:141], s[98:99] op_sel_hi:[1,0]
	v_pk_mul_f32 v[234:235], v[130:131], s[98:99] op_sel_hi:[1,0]
	v_pk_mul_f32 v[236:237], v[132:133], s[98:99] op_sel_hi:[1,0]
	v_pk_mul_f32 v[238:239], v[122:123], s[98:99] op_sel_hi:[1,0]
	v_pk_mul_f32 v[240:241], v[124:125], s[98:99] op_sel_hi:[1,0]
	v_pk_mul_f32 v[242:243], v[114:115], s[98:99] op_sel_hi:[1,0]
	v_pk_mul_f32 v[244:245], v[116:117], s[98:99] op_sel_hi:[1,0]
	v_exp_f32_e32 v230, v230
	v_exp_f32_e32 v231, v231
	v_exp_f32_e32 v232, v232
	v_exp_f32_e32 v233, v233
	v_exp_f32_e32 v234, v234
	v_exp_f32_e32 v235, v235
	v_exp_f32_e32 v236, v236
	v_exp_f32_e32 v237, v237
	v_exp_f32_e32 v238, v238
	v_exp_f32_e32 v239, v239
	v_exp_f32_e32 v240, v240
	v_exp_f32_e32 v241, v241
	v_exp_f32_e32 v242, v242
	v_exp_f32_e32 v243, v243
	v_exp_f32_e32 v244, v244
	v_exp_f32_e32 v245, v245
	v_pk_add_f32 v[230:231], v[230:231], 1.0 op_sel_hi:[1,0]
	v_pk_add_f32 v[232:233], v[232:233], 1.0 op_sel_hi:[1,0]
	v_pk_add_f32 v[234:235], v[234:235], 1.0 op_sel_hi:[1,0]
	v_pk_add_f32 v[236:237], v[236:237], 1.0 op_sel_hi:[1,0]
	v_pk_add_f32 v[238:239], v[238:239], 1.0 op_sel_hi:[1,0]
	v_pk_add_f32 v[240:241], v[240:241], 1.0 op_sel_hi:[1,0]
	v_pk_add_f32 v[242:243], v[242:243], 1.0 op_sel_hi:[1,0]
	v_pk_add_f32 v[244:245], v[244:245], 1.0 op_sel_hi:[1,0]
	v_rcp_f32_e32 v230, v230
	v_rcp_f32_e32 v231, v231
	v_rcp_f32_e32 v232, v232
	v_rcp_f32_e32 v233, v233
	v_rcp_f32_e32 v234, v234
	v_rcp_f32_e32 v235, v235
	v_rcp_f32_e32 v236, v236
	v_rcp_f32_e32 v237, v237
	v_rcp_f32_e32 v238, v238
	v_rcp_f32_e32 v239, v239
	v_rcp_f32_e32 v240, v240
	v_rcp_f32_e32 v241, v241
	v_rcp_f32_e32 v242, v242
	v_rcp_f32_e32 v243, v243
	v_rcp_f32_e32 v244, v244
	v_rcp_f32_e32 v245, v245
	v_pk_mul_f32 v[230:231], v[138:139], v[230:231]
	v_pk_mul_f32 v[232:233], v[140:141], v[232:233]
	v_pk_mul_f32 v[234:235], v[130:131], v[234:235]
	v_pk_mul_f32 v[236:237], v[132:133], v[236:237]
	v_pk_mul_f32 v[238:239], v[122:123], v[238:239]
	v_pk_mul_f32 v[240:241], v[124:125], v[240:241]
	v_pk_mul_f32 v[242:243], v[114:115], v[242:243]
	v_pk_mul_f32 v[244:245], v[116:117], v[244:245]
	v_pk_mul_f32 v[110:111], v[110:111], v[230:231]
	v_pk_mul_f32 v[112:113], v[112:113], v[232:233]
	v_pk_mul_f32 v[106:107], v[106:107], v[234:235]
	v_pk_mul_f32 v[108:109], v[108:109], v[236:237]
	v_pk_mul_f32 v[102:103], v[102:103], v[238:239]
	v_pk_mul_f32 v[104:105], v[104:105], v[240:241]
	v_pk_mul_f32 v[98:99], v[98:99], v[242:243]
	v_pk_mul_f32 v[100:101], v[100:101], v[244:245]
	v_med3_f32 v110, v110, s72, v197
	v_med3_f32 v111, v111, s72, v197
	v_med3_f32 v112, v112, s72, v197
	v_med3_f32 v113, v113, s72, v197
	v_med3_f32 v106, v106, s72, v197
	v_med3_f32 v107, v107, s72, v197
	v_med3_f32 v108, v108, s72, v197
	v_med3_f32 v109, v109, s72, v197
	v_med3_f32 v102, v102, s72, v197
	v_med3_f32 v103, v103, s72, v197
	v_med3_f32 v104, v104, s72, v197
	v_med3_f32 v105, v105, s72, v197
	v_med3_f32 v98, v98, s72, v197
	v_med3_f32 v99, v99, s72, v197
	v_med3_f32 v100, v100, s72, v197
	v_med3_f32 v101, v101, s72, v197
	v_cvt_pk_fp8_f32 v250, v110, v111
	v_cvt_pk_fp8_f32 v251, v106, v107
	v_cvt_pk_fp8_f32 v252, v102, v103
	v_cvt_pk_fp8_f32 v253, v98, v99
	v_add_u32_e32 v207, s73, v206
	v_add_u32_e32 v208, s74, v206
	v_cvt_pk_fp8_f32 v250, v112, v113 op_sel:[0,0,1]
	v_cvt_pk_fp8_f32 v251, v108, v109 op_sel:[0,0,1]
	v_cvt_pk_fp8_f32 v252, v104, v105 op_sel:[0,0,1]
	v_cvt_pk_fp8_f32 v253, v100, v101 op_sel:[0,0,1]
	s_nop 1
	global_store_dwordx2 v207, v[250:251], s[100:101]
	global_store_dwordx2 v208, v[252:253], s[100:101]
	v_pk_fma_f32 v[94:95], v[94:95], s[18:19], 0 op_sel_hi:[1,0,0]
	v_pk_fma_f32 v[96:97], v[96:97], s[18:19], 0 op_sel_hi:[1,0,0]
	v_pk_fma_f32 v[90:91], v[90:91], s[18:19], 0 op_sel_hi:[1,0,0]
	v_pk_fma_f32 v[92:93], v[92:93], s[18:19], 0 op_sel_hi:[1,0,0]
	v_pk_fma_f32 v[78:79], v[78:79], s[20:21], 0 op_sel_hi:[1,0,0]
	v_pk_fma_f32 v[80:81], v[80:81], s[20:21], 0 op_sel_hi:[1,0,0]
	v_pk_fma_f32 v[70:71], v[70:71], s[20:21], 0 op_sel_hi:[1,0,0]
	v_pk_fma_f32 v[72:73], v[72:73], s[20:21], 0 op_sel_hi:[1,0,0]
	v_pk_fma_f32 v[86:87], v[86:87], s[18:19], 0 op_sel_hi:[1,0,0]
	v_pk_fma_f32 v[88:89], v[88:89], s[18:19], 0 op_sel_hi:[1,0,0]
	v_pk_fma_f32 v[82:83], v[82:83], s[18:19], 0 op_sel_hi:[1,0,0]
	v_pk_fma_f32 v[84:85], v[84:85], s[18:19], 0 op_sel_hi:[1,0,0]
	v_pk_fma_f32 v[62:63], v[62:63], s[20:21], 0 op_sel_hi:[1,0,0]
	v_pk_fma_f32 v[64:65], v[64:65], s[20:21], 0 op_sel_hi:[1,0,0]
	v_pk_fma_f32 v[54:55], v[54:55], s[20:21], 0 op_sel_hi:[1,0,0]
	v_pk_fma_f32 v[56:57], v[56:57], s[20:21], 0 op_sel_hi:[1,0,0]
	v_pk_mul_f32 v[230:231], v[94:95], s[98:99] op_sel_hi:[1,0]
	v_pk_mul_f32 v[232:233], v[96:97], s[98:99] op_sel_hi:[1,0]
	v_pk_mul_f32 v[234:235], v[90:91], s[98:99] op_sel_hi:[1,0]
	v_pk_mul_f32 v[236:237], v[92:93], s[98:99] op_sel_hi:[1,0]
	v_pk_mul_f32 v[238:239], v[86:87], s[98:99] op_sel_hi:[1,0]
	v_pk_mul_f32 v[240:241], v[88:89], s[98:99] op_sel_hi:[1,0]
	v_pk_mul_f32 v[242:243], v[82:83], s[98:99] op_sel_hi:[1,0]
	v_pk_mul_f32 v[244:245], v[84:85], s[98:99] op_sel_hi:[1,0]
	v_exp_f32_e32 v230, v230
	v_exp_f32_e32 v231, v231
	v_exp_f32_e32 v232, v232
	v_exp_f32_e32 v233, v233
	v_exp_f32_e32 v234, v234
	v_exp_f32_e32 v235, v235
	v_exp_f32_e32 v236, v236
	v_exp_f32_e32 v237, v237
	v_exp_f32_e32 v238, v238
	v_exp_f32_e32 v239, v239
	v_exp_f32_e32 v240, v240
	v_exp_f32_e32 v241, v241
	v_exp_f32_e32 v242, v242
	v_exp_f32_e32 v243, v243
	v_exp_f32_e32 v244, v244
	v_exp_f32_e32 v245, v245
	v_pk_add_f32 v[230:231], v[230:231], 1.0 op_sel_hi:[1,0]
	v_pk_add_f32 v[232:233], v[232:233], 1.0 op_sel_hi:[1,0]
	v_pk_add_f32 v[234:235], v[234:235], 1.0 op_sel_hi:[1,0]
	v_pk_add_f32 v[236:237], v[236:237], 1.0 op_sel_hi:[1,0]
	v_pk_add_f32 v[238:239], v[238:239], 1.0 op_sel_hi:[1,0]
	v_pk_add_f32 v[240:241], v[240:241], 1.0 op_sel_hi:[1,0]
	v_pk_add_f32 v[242:243], v[242:243], 1.0 op_sel_hi:[1,0]
	v_pk_add_f32 v[244:245], v[244:245], 1.0 op_sel_hi:[1,0]
	v_rcp_f32_e32 v230, v230
	v_rcp_f32_e32 v231, v231
	v_rcp_f32_e32 v232, v232
	v_rcp_f32_e32 v233, v233
	v_rcp_f32_e32 v234, v234
	v_rcp_f32_e32 v235, v235
	v_rcp_f32_e32 v236, v236
	v_rcp_f32_e32 v237, v237
	v_rcp_f32_e32 v238, v238
	v_rcp_f32_e32 v239, v239
	v_rcp_f32_e32 v240, v240
	v_rcp_f32_e32 v241, v241
	v_rcp_f32_e32 v242, v242
	v_rcp_f32_e32 v243, v243
	v_rcp_f32_e32 v244, v244
	v_rcp_f32_e32 v245, v245
	v_pk_mul_f32 v[230:231], v[94:95], v[230:231]
	v_pk_mul_f32 v[232:233], v[96:97], v[232:233]
	v_pk_mul_f32 v[234:235], v[90:91], v[234:235]
	v_pk_mul_f32 v[236:237], v[92:93], v[236:237]
	v_pk_mul_f32 v[238:239], v[86:87], v[238:239]
	v_pk_mul_f32 v[240:241], v[88:89], v[240:241]
	v_pk_mul_f32 v[242:243], v[82:83], v[242:243]
	v_pk_mul_f32 v[244:245], v[84:85], v[244:245]
	v_pk_mul_f32 v[78:79], v[78:79], v[230:231]
	v_pk_mul_f32 v[80:81], v[80:81], v[232:233]
	v_pk_mul_f32 v[70:71], v[70:71], v[234:235]
	v_pk_mul_f32 v[72:73], v[72:73], v[236:237]
	v_pk_mul_f32 v[62:63], v[62:63], v[238:239]
	v_pk_mul_f32 v[64:65], v[64:65], v[240:241]
	v_pk_mul_f32 v[54:55], v[54:55], v[242:243]
	v_pk_mul_f32 v[56:57], v[56:57], v[244:245]
	v_med3_f32 v78, v78, s72, v197
	v_med3_f32 v79, v79, s72, v197
	v_med3_f32 v80, v80, s72, v197
	v_med3_f32 v81, v81, s72, v197
	v_med3_f32 v70, v70, s72, v197
	v_med3_f32 v71, v71, s72, v197
	v_med3_f32 v72, v72, s72, v197
	v_med3_f32 v73, v73, s72, v197
	v_med3_f32 v62, v62, s72, v197
	v_med3_f32 v63, v63, s72, v197
	v_med3_f32 v64, v64, s72, v197
	v_med3_f32 v65, v65, s72, v197
	v_med3_f32 v54, v54, s72, v197
	v_med3_f32 v55, v55, s72, v197
	v_med3_f32 v56, v56, s72, v197
	v_med3_f32 v57, v57, s72, v197
	v_cvt_pk_fp8_f32 v246, v78, v79
	v_cvt_pk_fp8_f32 v247, v70, v71
	v_cvt_pk_fp8_f32 v248, v62, v63
	v_cvt_pk_fp8_f32 v249, v54, v55
	v_add_u32_e32 v207, s75, v206
	v_add_u32_e32 v208, s76, v206
	v_cvt_pk_fp8_f32 v246, v80, v81 op_sel:[0,0,1]
	v_cvt_pk_fp8_f32 v247, v72, v73 op_sel:[0,0,1]
	v_cvt_pk_fp8_f32 v248, v64, v65 op_sel:[0,0,1]
	v_cvt_pk_fp8_f32 v249, v56, v57 op_sel:[0,0,1]
	s_nop 1
	global_store_dwordx2 v207, v[246:247], s[100:101]
	global_store_dwordx2 v208, v[248:249], s[100:101]
	v_pk_fma_f32 v[74:75], v[74:75], s[18:19], 0 op_sel_hi:[1,0,0]
	v_pk_fma_f32 v[76:77], v[76:77], s[18:19], 0 op_sel_hi:[1,0,0]
	v_pk_fma_f32 v[66:67], v[66:67], s[18:19], 0 op_sel_hi:[1,0,0]
	v_pk_fma_f32 v[68:69], v[68:69], s[18:19], 0 op_sel_hi:[1,0,0]
	v_pk_fma_f32 v[46:47], v[46:47], s[20:21], 0 op_sel_hi:[1,0,0]
	v_pk_fma_f32 v[48:49], v[48:49], s[20:21], 0 op_sel_hi:[1,0,0]
	v_pk_fma_f32 v[42:43], v[42:43], s[20:21], 0 op_sel_hi:[1,0,0]
	v_pk_fma_f32 v[44:45], v[44:45], s[20:21], 0 op_sel_hi:[1,0,0]
	v_pk_fma_f32 v[58:59], v[58:59], s[18:19], 0 op_sel_hi:[1,0,0]
	v_pk_fma_f32 v[60:61], v[60:61], s[18:19], 0 op_sel_hi:[1,0,0]
	v_pk_fma_f32 v[50:51], v[50:51], s[18:19], 0 op_sel_hi:[1,0,0]
	v_pk_fma_f32 v[52:53], v[52:53], s[18:19], 0 op_sel_hi:[1,0,0]
	v_pk_fma_f32 v[38:39], v[38:39], s[20:21], 0 op_sel_hi:[1,0,0]
	v_pk_fma_f32 v[40:41], v[40:41], s[20:21], 0 op_sel_hi:[1,0,0]
	v_pk_fma_f32 v[34:35], v[34:35], s[20:21], 0 op_sel_hi:[1,0,0]
	v_pk_fma_f32 v[36:37], v[36:37], s[20:21], 0 op_sel_hi:[1,0,0]
	v_pk_mul_f32 v[230:231], v[74:75], s[98:99] op_sel_hi:[1,0]
	v_pk_mul_f32 v[232:233], v[76:77], s[98:99] op_sel_hi:[1,0]
	v_pk_mul_f32 v[234:235], v[66:67], s[98:99] op_sel_hi:[1,0]
	v_pk_mul_f32 v[236:237], v[68:69], s[98:99] op_sel_hi:[1,0]
	v_pk_mul_f32 v[238:239], v[58:59], s[98:99] op_sel_hi:[1,0]
	v_pk_mul_f32 v[240:241], v[60:61], s[98:99] op_sel_hi:[1,0]
	v_pk_mul_f32 v[242:243], v[50:51], s[98:99] op_sel_hi:[1,0]
	v_pk_mul_f32 v[244:245], v[52:53], s[98:99] op_sel_hi:[1,0]
	v_exp_f32_e32 v230, v230
	v_exp_f32_e32 v231, v231
	v_exp_f32_e32 v232, v232
	v_exp_f32_e32 v233, v233
	v_exp_f32_e32 v234, v234
	v_exp_f32_e32 v235, v235
	v_exp_f32_e32 v236, v236
	v_exp_f32_e32 v237, v237
	v_exp_f32_e32 v238, v238
	v_exp_f32_e32 v239, v239
	v_exp_f32_e32 v240, v240
	v_exp_f32_e32 v241, v241
	v_exp_f32_e32 v242, v242
	v_exp_f32_e32 v243, v243
	v_exp_f32_e32 v244, v244
	v_exp_f32_e32 v245, v245
	v_pk_add_f32 v[230:231], v[230:231], 1.0 op_sel_hi:[1,0]
	v_pk_add_f32 v[232:233], v[232:233], 1.0 op_sel_hi:[1,0]
	v_pk_add_f32 v[234:235], v[234:235], 1.0 op_sel_hi:[1,0]
	v_pk_add_f32 v[236:237], v[236:237], 1.0 op_sel_hi:[1,0]
	v_pk_add_f32 v[238:239], v[238:239], 1.0 op_sel_hi:[1,0]
	v_pk_add_f32 v[240:241], v[240:241], 1.0 op_sel_hi:[1,0]
	v_pk_add_f32 v[242:243], v[242:243], 1.0 op_sel_hi:[1,0]
	v_pk_add_f32 v[244:245], v[244:245], 1.0 op_sel_hi:[1,0]
	v_rcp_f32_e32 v230, v230
	v_rcp_f32_e32 v231, v231
	v_rcp_f32_e32 v232, v232
	v_rcp_f32_e32 v233, v233
	v_rcp_f32_e32 v234, v234
	v_rcp_f32_e32 v235, v235
	v_rcp_f32_e32 v236, v236
	v_rcp_f32_e32 v237, v237
	v_rcp_f32_e32 v238, v238
	v_rcp_f32_e32 v239, v239
	v_rcp_f32_e32 v240, v240
	v_rcp_f32_e32 v241, v241
	v_rcp_f32_e32 v242, v242
	v_rcp_f32_e32 v243, v243
	v_rcp_f32_e32 v244, v244
	v_rcp_f32_e32 v245, v245
	v_pk_mul_f32 v[230:231], v[74:75], v[230:231]
	v_pk_mul_f32 v[232:233], v[76:77], v[232:233]
	v_pk_mul_f32 v[234:235], v[66:67], v[234:235]
	v_pk_mul_f32 v[236:237], v[68:69], v[236:237]
	v_pk_mul_f32 v[238:239], v[58:59], v[238:239]
	v_pk_mul_f32 v[240:241], v[60:61], v[240:241]
	v_pk_mul_f32 v[242:243], v[50:51], v[242:243]
	v_pk_mul_f32 v[244:245], v[52:53], v[244:245]
	v_pk_mul_f32 v[46:47], v[46:47], v[230:231]
	v_pk_mul_f32 v[48:49], v[48:49], v[232:233]
	v_pk_mul_f32 v[42:43], v[42:43], v[234:235]
	v_pk_mul_f32 v[44:45], v[44:45], v[236:237]
	v_pk_mul_f32 v[38:39], v[38:39], v[238:239]
	v_pk_mul_f32 v[40:41], v[40:41], v[240:241]
	v_pk_mul_f32 v[34:35], v[34:35], v[242:243]
	v_pk_mul_f32 v[36:37], v[36:37], v[244:245]
	v_med3_f32 v46, v46, s72, v197
	v_med3_f32 v47, v47, s72, v197
	v_med3_f32 v48, v48, s72, v197
	v_med3_f32 v49, v49, s72, v197
	v_med3_f32 v42, v42, s72, v197
	v_med3_f32 v43, v43, s72, v197
	v_med3_f32 v44, v44, s72, v197
	v_med3_f32 v45, v45, s72, v197
	v_med3_f32 v38, v38, s72, v197
	v_med3_f32 v39, v39, s72, v197
	v_med3_f32 v40, v40, s72, v197
	v_med3_f32 v41, v41, s72, v197
	v_med3_f32 v34, v34, s72, v197
	v_med3_f32 v35, v35, s72, v197
	v_med3_f32 v36, v36, s72, v197
	v_med3_f32 v37, v37, s72, v197
	v_cvt_pk_fp8_f32 v250, v46, v47
	v_cvt_pk_fp8_f32 v251, v42, v43
	v_cvt_pk_fp8_f32 v252, v38, v39
	v_cvt_pk_fp8_f32 v253, v34, v35
	v_add_u32_e32 v207, s77, v206
	v_add_u32_e32 v208, 0xf2000, v206
	v_cvt_pk_fp8_f32 v250, v48, v49 op_sel:[0,0,1]
	v_cvt_pk_fp8_f32 v251, v44, v45 op_sel:[0,0,1]
	v_cvt_pk_fp8_f32 v252, v40, v41 op_sel:[0,0,1]
	v_cvt_pk_fp8_f32 v253, v36, v37 op_sel:[0,0,1]
	s_nop 1
	global_store_dwordx2 v207, v[250:251], s[100:101]
	global_store_dwordx2 v208, v[252:253], s[100:101]
	s_andn2_b64 vcc, exec, s[2:3]
	s_mov_b64 s[2:3], -1
	s_cbranch_vccnz .LBB0_2928
	s_andn2_b64 vcc, exec, s[10:11]
	s_cbranch_vccnz .LBB0_2927
	s_barrier
	s_branch .LBB0_2927
